# combo17 + phase 2 attention-V transpose thread map changed so transposed stores fill whole 128-byte lines
# speedup vs baseline: 1.0325x; 1.0170x over previous
.LBB0_445:
	v_or_b32_e32 v164, s22, v136
	v_or_b32_e32 v165, s23, v137
	v_mad_u64_u32 v[58:59], s[22:23], v164, s93, v[134:135]
	v_mov_b32_e32 v60, v59
	v_mad_u64_u32 v[60:61], s[22:23], v165, s93, v[60:61]
	v_mov_b32_e32 v59, v60
	global_load_dwordx4 v[114:117], v[58:59], off
	v_add_co_u32_e32 v62, vcc, s97, v58
	s_mov_b32 s22, 0x9000
	s_nop 0
	v_addc_co_u32_e32 v63, vcc, 0, v60, vcc
	global_load_dwordx4 v[118:121], v[62:63], off offset:3072
	v_add_co_u32_e32 v62, vcc, s22, v58
	s_mov_b32 s22, 0xe000
	s_nop 0
	v_addc_co_u32_e32 v63, vcc, 0, v60, vcc
	global_load_dwordx4 v[106:109], v[62:63], off offset:2048
	v_add_co_u32_e32 v62, vcc, s22, v58
	s_mov_b32 s22, 0x13000
	s_nop 0
	v_addc_co_u32_e32 v63, vcc, 0, v60, vcc
	global_load_dwordx4 v[110:113], v[62:63], off offset:1024
	v_add_co_u32_e32 v62, vcc, s22, v58
	v_pk_mul_f32 v[220:221], v[160:161], v[180:181]
	s_nop 0
	v_addc_co_u32_e32 v63, vcc, 0, v60, vcc
	global_load_dwordx4 v[98:101], v[62:63], off
	v_mov_b32_e32 v183, v181
	v_pk_mul_f32 v[224:225], v[42:43], v[182:183]
	v_add_f32_e32 v126, v221, v220
	v_pk_mul_f32 v[200:201], v[144:145], v[166:167]
	s_mov_b32 s22, 0x17000
	v_add_co_u32_e32 v62, vcc, s22, v58
	s_mov_b32 s22, 0x1c000
	s_nop 0
	v_addc_co_u32_e32 v63, vcc, 0, v60, vcc
	global_load_dwordx4 v[102:105], v[62:63], off offset:3072
	v_add_co_u32_e32 v62, vcc, s22, v58
	v_pk_mul_f32 v[222:223], v[162:163], v[178:179]
	v_mov_b32_e32 v185, v179
	v_addc_co_u32_e32 v63, vcc, 0, v60, vcc
	s_mov_b32 s22, 0x21000
	global_load_dwordx4 v[90:93], v[62:63], off offset:2048
	v_add_co_u32_e32 v62, vcc, s22, v58
	s_mov_b32 s22, 0x26000
	s_nop 0
	v_addc_co_u32_e32 v63, vcc, 0, v60, vcc
	global_load_dwordx4 v[94:97], v[62:63], off offset:1024
	v_add_co_u32_e32 v62, vcc, s22, v58
	s_mov_b32 s22, 0x2a000
	s_nop 0
	v_addc_co_u32_e32 v63, vcc, 0, v60, vcc
	global_load_dwordx4 v[82:85], v[62:63], off
	v_add_co_u32_e32 v62, vcc, s22, v58
	s_mov_b32 s22, 0x2f000
	s_nop 0
	v_addc_co_u32_e32 v63, vcc, 0, v60, vcc
	global_load_dwordx4 v[86:89], v[62:63], off offset:3072
	v_add_co_u32_e32 v62, vcc, s22, v58
	s_mov_b32 s22, 0x34000
	s_nop 0
	v_addc_co_u32_e32 v63, vcc, 0, v60, vcc
	global_load_dwordx4 v[74:77], v[62:63], off offset:2048
	v_add_co_u32_e32 v62, vcc, s22, v58
	s_mov_b32 s22, 0x39000
	s_nop 0
	v_addc_co_u32_e32 v63, vcc, 0, v60, vcc
	global_load_dwordx4 v[78:81], v[62:63], off offset:1024
	v_add_co_u32_e32 v62, vcc, s22, v58
	s_mov_b32 s22, 0x3d000
	s_nop 0
	v_addc_co_u32_e32 v63, vcc, 0, v60, vcc
	global_load_dwordx4 v[70:73], v[62:63], off
	s_waitcnt vmcnt(12)
	v_lshlrev_b32_e32 v180, 16, v114
	v_mov_b32_e32 v183, v180
	v_pk_mul_f32 v[226:227], v[158:159], v[182:183]
	v_and_b32_e32 v178, 0xffff0000, v114
	v_add_f32_e32 v126, v226, v126
	v_add_f32_e32 v126, v126, v227
	v_mul_f32_e32 v166, 0xbfb8aa3b, v126
	v_exp_f32_e32 v166, v166
	s_waitcnt vmcnt(11)
	v_lshlrev_b32_e32 v181, 16, v118
	v_pk_mul_f32 v[220:221], v[158:159], v[180:181]
	v_add_f32_e32 v114, v223, v222
	v_add_f32_e32 v166, 1.0, v166
	v_rcp_f32_e32 v166, v166
	v_and_b32_e32 v179, 0xffff0000, v118
	v_add_co_u32_e32 v62, vcc, s22, v58
	v_mul_f32_e32 v126, v126, v166
	v_mul_f32_e32 v166, 0x3d800000, v126
	v_cndmask_b32_e64 v166, v126, v166, s[18:19]
	v_add_f32_e32 v126, v224, v225
	v_add_f32_e32 v126, v126, v220
	v_add_f32_e32 v126, v126, v221
	v_pk_mul_f32 v[220:221], v[38:39], v[184:185]
	v_mov_b32_e32 v185, v178
	v_pk_mul_f32 v[224:225], v[50:51], v[184:185]
	v_addc_co_u32_e32 v63, vcc, 0, v60, vcc
	v_add_f32_e32 v114, v224, v114
	v_add_f32_e32 v114, v114, v225
	v_mul_f32_e32 v118, 0xbfb8aa3b, v114
	v_exp_f32_e32 v118, v118
	s_mov_b32 s22, 0x42000
	v_add_co_u32_e32 v66, vcc, s22, v58
	v_add_f32_e32 v118, 1.0, v118
	v_rcp_f32_e32 v118, v118
	v_addc_co_u32_e32 v67, vcc, 0, v60, vcc
	s_mov_b32 s22, 0x47000
	v_mul_f32_e32 v114, v114, v118
	v_mul_f32_e32 v118, 0x3d800000, v114
	v_cndmask_b32_e64 v114, v114, v118, s[18:19]
	v_pk_mul_f32 v[222:223], v[50:51], v[178:179]
	v_add_f32_e32 v118, v220, v221
	v_add_co_u32_e32 v58, vcc, s22, v58
	v_add_f32_e32 v118, v118, v222
	s_nop 0
	v_addc_co_u32_e32 v59, vcc, 0, v60, vcc
	v_add_f32_e32 v118, v118, v223
	global_load_dwordx4 v[62:65], v[62:63], off offset:3072
	v_pk_mul_f32 v[202:203], v[142:143], v[168:169]
	global_load_dwordx4 v[66:69], v[66:67], off offset:2048
	v_mul_f32_e32 v168, 0xbfb8aa3b, v126
	global_load_dwordx4 v[58:61], v[58:59], off offset:1024
	v_cvt_pk_bf16_f32 v114, v166, v114
	v_mul_f32_e32 v166, 0xbfb8aa3b, v118
	v_exp_f32_e32 v166, v166
	v_exp_f32_e32 v168, v168
	v_pk_mul_f32 v[210:211], v[154:155], v[176:177]
	v_mov_b32_e32 v187, v177
	v_add_f32_e32 v166, 1.0, v166
	v_rcp_f32_e32 v166, v166
	v_add_f32_e32 v168, 1.0, v168
	v_rcp_f32_e32 v168, v168
	v_lshlrev_b32_e32 v176, 16, v115
	v_mul_f32_e32 v118, v118, v166
	v_mul_f32_e32 v166, 0x3d800000, v118
	v_pk_mul_f32 v[220:221], v[44:45], v[186:187]
	v_mov_b32_e32 v187, v176
	v_cndmask_b32_e64 v166, v118, v166, s[18:19]
	v_pk_mul_f32 v[222:223], v[152:153], v[186:187]
	v_add_f32_e32 v118, v211, v210
	v_mul_f32_e32 v126, v126, v168
	v_add_f32_e32 v118, v222, v118
	v_mul_f32_e32 v168, 0x3d800000, v126
	v_add_f32_e32 v118, v118, v223
	v_cndmask_b32_e64 v126, v126, v168, s[18:19]
	v_mul_f32_e32 v168, 0xbfb8aa3b, v118
	v_exp_f32_e32 v168, v168
	v_lshlrev_b32_e32 v177, 16, v119
	v_pk_mul_f32 v[210:211], v[152:153], v[176:177]
	v_pk_mul_f32 v[204:205], v[150:151], v[170:171]
	v_add_f32_e32 v168, 1.0, v168
	v_rcp_f32_e32 v168, v168
	v_pk_mul_f32 v[208:209], v[156:157], v[174:175]
	v_mov_b32_e32 v189, v175
	v_and_b32_e32 v119, 0xffff0000, v119
	v_mul_f32_e32 v118, v118, v168
	v_mul_f32_e32 v168, 0x3d800000, v118
	v_cndmask_b32_e64 v168, v118, v168, s[18:19]
	v_add_f32_e32 v118, v220, v221
	v_add_f32_e32 v118, v118, v210
	v_add_f32_e32 v118, v118, v211
	v_mul_f32_e32 v170, 0xbfb8aa3b, v118
	v_exp_f32_e32 v170, v170
	v_pk_mul_f32 v[210:211], v[40:41], v[188:189]
	v_pk_mul_f32 v[206:207], v[148:149], v[172:173]
	v_mov_b32_e32 v191, v173
	v_add_f32_e32 v170, 1.0, v170
	v_rcp_f32_e32 v170, v170
	v_lshlrev_b32_e32 v172, 16, v116
	v_lshlrev_b32_e32 v173, 16, v120
	v_mov_b32_e32 v195, v169
	v_mul_f32_e32 v118, v118, v170
	v_mul_f32_e32 v170, 0x3d800000, v118
	v_cndmask_b32_e64 v174, v118, v170, s[18:19]
	v_and_b32_e32 v118, 0xffff0000, v115
	v_mov_b32_e32 v189, v118
	v_pk_mul_f32 v[220:221], v[52:53], v[188:189]
	v_add_f32_e32 v115, v209, v208
	v_add_f32_e32 v115, v220, v115
	v_add_f32_e32 v115, v115, v221
	v_mul_f32_e32 v170, 0xbfb8aa3b, v115
	v_exp_f32_e32 v170, v170
	v_pk_mul_f32 v[208:209], v[52:53], v[118:119]
	v_lshlrev_b32_e32 v169, 16, v121
	v_lshlrev_b64 v[164:165], 11, v[164:165]
	v_add_f32_e32 v170, 1.0, v170
	v_rcp_f32_e32 v170, v170
	v_lshl_add_u64 v[198:199], v[138:139], 0, v[164:165]
	v_and_b32_e32 v121, 0xffff0000, v121
	s_mov_b64 s[22:23], 16
	v_mul_f32_e32 v115, v115, v170
	v_mul_f32_e32 v170, 0x3d800000, v115
	v_cndmask_b32_e64 v115, v115, v170, s[18:19]
	v_cvt_pk_bf16_f32 v115, v168, v115
	v_add_f32_e32 v168, v210, v211
	v_add_f32_e32 v168, v168, v208
	v_add_f32_e32 v168, v168, v209
	v_mul_f32_e32 v170, 0xbfb8aa3b, v168
	v_exp_f32_e32 v170, v170
	v_pk_mul_f32 v[208:209], v[46:47], v[190:191]
	v_mov_b32_e32 v191, v172
	v_pk_mul_f32 v[210:211], v[146:147], v[190:191]
	v_add_f32_e32 v170, 1.0, v170
	v_rcp_f32_e32 v170, v170
	s_andn2_b64 vcc, exec, s[20:21]
	s_mov_b64 s[20:21], 0
	v_mul_f32_e32 v168, v168, v170
	v_mul_f32_e32 v170, 0x3d800000, v168
	v_cndmask_b32_e64 v175, v168, v170, s[18:19]
	v_add_f32_e32 v168, v207, v206
	v_add_f32_e32 v168, v210, v168
	v_add_f32_e32 v168, v168, v211
	v_mul_f32_e32 v170, 0xbfb8aa3b, v168
	v_exp_f32_e32 v170, v170
	v_pk_mul_f32 v[206:207], v[146:147], v[172:173]
	v_add_f32_e32 v170, 1.0, v170
	v_rcp_f32_e32 v170, v170
	s_nop 0
	v_mul_f32_e32 v168, v168, v170
	v_mul_f32_e32 v170, 0x3d800000, v168
	v_cndmask_b32_e64 v168, v168, v170, s[18:19]
	v_add_f32_e32 v170, v208, v209
	v_add_f32_e32 v170, v170, v206
	v_add_f32_e32 v170, v170, v207
	v_mul_f32_e32 v193, 0xbfb8aa3b, v170
	v_exp_f32_e32 v193, v193
	s_nop 0
	v_add_f32_e32 v193, 1.0, v193
	v_rcp_f32_e32 v193, v193
	s_nop 0
	v_mul_f32_e32 v170, v170, v193
	v_mul_f32_e32 v193, 0x3d800000, v170
	v_cndmask_b32_e64 v206, v170, v193, s[18:19]
	v_mov_b32_e32 v193, v171
	v_and_b32_e32 v170, 0xffff0000, v116
	v_pk_mul_f32 v[208:209], v[34:35], v[192:193]
	v_mov_b32_e32 v193, v170
	v_pk_mul_f32 v[210:211], v[54:55], v[192:193]
	v_add_f32_e32 v116, v205, v204
	v_add_f32_e32 v116, v210, v116
	v_add_f32_e32 v116, v116, v211
	v_and_b32_e32 v171, 0xffff0000, v120
	v_mul_f32_e32 v120, 0xbfb8aa3b, v116
	v_exp_f32_e32 v120, v120
	v_pk_mul_f32 v[204:205], v[54:55], v[170:171]
	v_add_f32_e32 v120, 1.0, v120
	v_rcp_f32_e32 v120, v120
	s_nop 0
	v_mul_f32_e32 v116, v116, v120
	v_mul_f32_e32 v120, 0x3d800000, v116
	v_cndmask_b32_e64 v116, v116, v120, s[18:19]
	v_add_f32_e32 v120, v208, v209
	v_add_f32_e32 v120, v120, v204
	v_add_f32_e32 v120, v120, v205
	v_cvt_pk_bf16_f32 v116, v168, v116
	v_mul_f32_e32 v168, 0xbfb8aa3b, v120
	v_exp_f32_e32 v168, v168
	v_pk_mul_f32 v[204:205], v[48:49], v[194:195]
	v_add_f32_e32 v168, 1.0, v168
	v_rcp_f32_e32 v168, v168
	s_nop 0
	v_mul_f32_e32 v120, v120, v168
	v_mul_f32_e32 v168, 0x3d800000, v120
	v_cndmask_b32_e64 v207, v120, v168, s[18:19]
	v_lshlrev_b32_e32 v168, 16, v117
	v_mov_b32_e32 v195, v168
	v_pk_mul_f32 v[208:209], v[140:141], v[194:195]
	v_add_f32_e32 v120, v203, v202
	v_add_f32_e32 v120, v208, v120
	v_add_f32_e32 v120, v120, v209
	v_mul_f32_e32 v197, 0xbfb8aa3b, v120
	v_exp_f32_e32 v197, v197
	v_pk_mul_f32 v[202:203], v[140:141], v[168:169]
	v_add_f32_e32 v197, 1.0, v197
	v_rcp_f32_e32 v197, v197
	s_nop 0
	v_mul_f32_e32 v120, v120, v197
	v_mul_f32_e32 v197, 0x3d800000, v120
	v_cndmask_b32_e64 v208, v120, v197, s[18:19]
	v_add_f32_e32 v120, v204, v205
	v_add_f32_e32 v120, v120, v202
	v_add_f32_e32 v120, v120, v203
	v_mul_f32_e32 v197, 0xbfb8aa3b, v120
	v_exp_f32_e32 v197, v197
	s_nop 0
	v_add_f32_e32 v197, 1.0, v197
	v_rcp_f32_e32 v197, v197
	s_nop 0
	v_mul_f32_e32 v120, v120, v197
	v_mul_f32_e32 v197, 0x3d800000, v120
	v_cndmask_b32_e64 v209, v120, v197, s[18:19]
	v_mov_b32_e32 v197, v167
	v_and_b32_e32 v120, 0xffff0000, v117
	v_pk_mul_f32 v[202:203], v[36:37], v[196:197]
	v_mov_b32_e32 v197, v120
	v_pk_mul_f32 v[204:205], v[56:57], v[196:197]
	v_add_f32_e32 v117, v201, v200
	v_add_f32_e32 v117, v204, v117
	v_add_f32_e32 v117, v117, v205
	v_mul_f32_e32 v167, 0xbfb8aa3b, v117
	v_exp_f32_e32 v167, v167
	v_pk_mul_f32 v[200:201], v[154:155], v[186:187]
	v_pk_mul_f32 v[186:187], v[148:149], v[190:191]
	v_add_f32_e32 v167, 1.0, v167
	v_rcp_f32_e32 v167, v167
	v_add_f32_e32 v186, v186, v187
	v_mul_f32_e32 v117, v117, v167
	v_mul_f32_e32 v167, 0x3d800000, v117
	v_cndmask_b32_e64 v117, v117, v167, s[18:19]
	v_cvt_pk_bf16_f32 v117, v208, v117
	global_store_dwordx4 v[198:199], v[114:117], off
	v_pk_mul_f32 v[198:199], v[156:157], v[188:189]
	v_pk_mul_f32 v[188:189], v[160:161], v[180:181]
	v_pk_mul_f32 v[114:115], v[56:57], v[120:121]
	v_add_f32_e32 v116, v202, v203
	v_add_f32_e32 v114, v116, v114
	v_add_f32_e32 v114, v114, v115
	v_mul_f32_e32 v115, 0xbfb8aa3b, v114
	v_exp_f32_e32 v115, v115
	v_pk_mul_f32 v[202:203], v[162:163], v[184:185]
	v_pk_mul_f32 v[184:185], v[150:151], v[192:193]
	v_mov_b32_e32 v167, v165
	v_add_f32_e32 v115, 1.0, v115
	v_rcp_f32_e32 v115, v115
	s_nop 0
	v_mul_f32_e32 v114, v114, v115
	v_mul_f32_e32 v115, 0x3d800000, v114
	v_cndmask_b32_e64 v117, v114, v115, s[18:19]
	v_cvt_pk_bf16_f32 v114, v126, v166
	v_cvt_pk_bf16_f32 v115, v174, v175
	v_pk_mul_f32 v[174:175], v[160:161], v[182:183]
	s_waitcnt vmcnt(13)
	v_lshlrev_b32_e32 v183, 16, v110
	v_lshlrev_b32_e32 v182, 16, v106
	v_pk_mov_b32 v[180:181], v[180:181], v[182:183] op_sel:[1,0]
	v_add_f32_e32 v126, v174, v175
	v_pk_mul_f32 v[190:191], v[158:159], v[180:181]
	v_or_b32_e32 v166, 0x800, v164
	v_add_f32_e32 v126, v126, v190
	v_add_f32_e32 v126, v126, v191
	v_mul_f32_e32 v174, 0xbfb8aa3b, v126
	v_exp_f32_e32 v174, v174
	v_pk_mul_f32 v[190:191], v[162:163], v[178:179]
	v_cvt_pk_bf16_f32 v116, v206, v207
	v_cvt_pk_bf16_f32 v117, v209, v117
	v_add_f32_e32 v174, 1.0, v174
	v_rcp_f32_e32 v174, v174
	v_lshl_add_u64 v[166:167], v[138:139], 0, v[166:167]
	global_store_dwordx4 v[166:167], v[114:117], off
	v_pk_mul_f32 v[166:167], v[142:143], v[194:195]
	v_mul_f32_e32 v126, v126, v174
	v_mul_f32_e32 v174, 0x3d800000, v126
	v_cndmask_b32_e64 v192, v126, v174, s[18:19]
	v_pk_mul_f32 v[174:175], v[158:159], v[182:183]
	v_add_f32_e32 v126, v188, v189
	v_add_f32_e32 v126, v126, v174
	v_add_f32_e32 v126, v126, v175
	v_mul_f32_e32 v174, 0xbfb8aa3b, v126
	v_exp_f32_e32 v174, v174
	v_and_b32_e32 v175, 0xffff0000, v110
	v_pk_mul_f32 v[116:117], v[144:145], v[196:197]
	v_or_b32_e32 v114, 0x1000, v164
	v_add_f32_e32 v174, 1.0, v174
	v_rcp_f32_e32 v174, v174
	v_mov_b32_e32 v115, v165
	v_lshl_add_u64 v[114:115], v[138:139], 0, v[114:115]
	v_mul_f32_e32 v126, v126, v174
	v_mul_f32_e32 v174, 0x3d800000, v126
	v_cndmask_b32_e64 v126, v126, v174, s[18:19]
	v_and_b32_e32 v174, 0xffff0000, v106
	v_pk_mov_b32 v[188:189], v[178:179], v[174:175] op_sel:[1,0]
	v_add_f32_e32 v106, v202, v203
	v_pk_mul_f32 v[178:179], v[50:51], v[188:189]
	s_nop 0
	v_add_f32_e32 v106, v106, v178
	v_add_f32_e32 v106, v106, v179
	v_mul_f32_e32 v110, 0xbfb8aa3b, v106
	v_exp_f32_e32 v110, v110
	v_pk_mul_f32 v[178:179], v[50:51], v[174:175]
	v_add_f32_e32 v110, 1.0, v110
	v_rcp_f32_e32 v110, v110
	s_nop 0
	v_mul_f32_e32 v106, v106, v110
	v_mul_f32_e32 v110, 0x3d800000, v106
	v_cndmask_b32_e64 v106, v106, v110, s[18:19]
	v_add_f32_e32 v110, v190, v191
	v_add_f32_e32 v110, v110, v178
	v_add_f32_e32 v110, v110, v179
	v_mul_f32_e32 v178, 0xbfb8aa3b, v110
	v_exp_f32_e32 v178, v178
	v_lshlrev_b32_e32 v179, 16, v111
	v_cvt_pk_bf16_f32 v106, v192, v106
	v_pk_mul_f32 v[192:193], v[154:155], v[176:177]
	v_add_f32_e32 v178, 1.0, v178
	v_rcp_f32_e32 v178, v178
	v_and_b32_e32 v111, 0xffff0000, v111
	v_mul_f32_e32 v110, v110, v178
	v_mul_f32_e32 v178, 0x3d800000, v110
	v_cndmask_b32_e64 v196, v110, v178, s[18:19]
	v_lshlrev_b32_e32 v178, 16, v107
	v_pk_mov_b32 v[190:191], v[176:177], v[178:179] op_sel:[1,0]
	v_add_f32_e32 v110, v200, v201
	v_pk_mul_f32 v[176:177], v[152:153], v[190:191]
	s_nop 0
	v_add_f32_e32 v110, v110, v176
	v_add_f32_e32 v110, v110, v177
	v_mul_f32_e32 v176, 0xbfb8aa3b, v110
	v_exp_f32_e32 v176, v176
	s_nop 0
	v_add_f32_e32 v176, 1.0, v176
	v_rcp_f32_e32 v176, v176
	s_nop 0
	v_mul_f32_e32 v110, v110, v176
	v_mul_f32_e32 v176, 0x3d800000, v110
	v_cndmask_b32_e64 v194, v110, v176, s[18:19]
	v_pk_mul_f32 v[176:177], v[152:153], v[178:179]
	v_add_f32_e32 v110, v192, v193
	v_add_f32_e32 v110, v110, v176
	v_add_f32_e32 v110, v110, v177
	v_mul_f32_e32 v176, 0xbfb8aa3b, v110
	v_exp_f32_e32 v176, v176
	s_nop 0
	v_add_f32_e32 v176, 1.0, v176
	v_rcp_f32_e32 v176, v176
	s_nop 0
	v_mul_f32_e32 v110, v110, v176
	v_mul_f32_e32 v176, 0x3d800000, v110
	v_cndmask_b32_e64 v197, v110, v176, s[18:19]
	v_and_b32_e32 v110, 0xffff0000, v107
	v_pk_mov_b32 v[192:193], v[118:119], v[110:111] op_sel:[1,0]
	v_pk_mul_f32 v[176:177], v[156:157], v[118:119]
	v_pk_mul_f32 v[118:119], v[52:53], v[192:193]
	v_add_f32_e32 v107, v198, v199
	v_add_f32_e32 v107, v107, v118
	v_add_f32_e32 v107, v107, v119
	v_mul_f32_e32 v118, 0xbfb8aa3b, v107
	v_exp_f32_e32 v118, v118
	v_add_f32_e32 v176, v176, v177
	v_lshlrev_b32_e32 v177, 16, v112
	v_add_f32_e32 v118, 1.0, v118
	v_rcp_f32_e32 v118, v118
	s_nop 0
	v_mul_f32_e32 v107, v107, v118
	v_mul_f32_e32 v118, 0x3d800000, v107
	v_cndmask_b32_e64 v107, v107, v118, s[18:19]
	v_pk_mul_f32 v[118:119], v[52:53], v[110:111]
	v_cvt_pk_bf16_f32 v107, v194, v107
	s_nop 0
	v_add_f32_e32 v118, v176, v118
	v_add_f32_e32 v118, v118, v119
	v_mul_f32_e32 v119, 0xbfb8aa3b, v118
	v_exp_f32_e32 v119, v119
	v_lshlrev_b32_e32 v176, 16, v108
	v_add_f32_e32 v119, 1.0, v119
	v_rcp_f32_e32 v119, v119
	s_nop 0
	v_mul_f32_e32 v118, v118, v119
	v_mul_f32_e32 v119, 0x3d800000, v118
	v_cndmask_b32_e64 v200, v118, v119, s[18:19]
	v_pk_mul_f32 v[118:119], v[148:149], v[172:173]
	v_pk_mov_b32 v[172:173], v[172:173], v[176:177] op_sel:[1,0]
	v_add_f32_e32 v118, v118, v119
	v_pk_mul_f32 v[194:195], v[146:147], v[172:173]
	s_nop 0
	v_add_f32_e32 v186, v186, v194
	v_add_f32_e32 v186, v186, v195
	v_mul_f32_e32 v187, 0xbfb8aa3b, v186
	v_exp_f32_e32 v187, v187
	s_nop 0
	v_add_f32_e32 v187, 1.0, v187
	v_rcp_f32_e32 v187, v187
	s_nop 0
	v_mul_f32_e32 v186, v186, v187
	v_mul_f32_e32 v187, 0x3d800000, v186
	v_cndmask_b32_e64 v198, v186, v187, s[18:19]
	v_pk_mul_f32 v[186:187], v[146:147], v[176:177]
	s_nop 0
	v_add_f32_e32 v118, v118, v186
	v_add_f32_e32 v118, v118, v187
	v_mul_f32_e32 v119, 0xbfb8aa3b, v118
	v_exp_f32_e32 v119, v119
	v_pk_mul_f32 v[186:187], v[150:151], v[170:171]
	v_add_f32_e32 v119, 1.0, v119
	v_rcp_f32_e32 v119, v119
	s_nop 0
	v_mul_f32_e32 v118, v118, v119
	v_mul_f32_e32 v119, 0x3d800000, v118
	v_cndmask_b32_e64 v201, v118, v119, s[18:19]
	v_and_b32_e32 v119, 0xffff0000, v112
	v_and_b32_e32 v118, 0xffff0000, v108
	v_pk_mov_b32 v[194:195], v[170:171], v[118:119] op_sel:[1,0]
	v_add_f32_e32 v108, v184, v185
	v_pk_mul_f32 v[170:171], v[54:55], v[194:195]
	v_pk_mul_f32 v[184:185], v[142:143], v[168:169]
	v_add_f32_e32 v108, v108, v170
	v_add_f32_e32 v108, v108, v171
	v_mul_f32_e32 v112, 0xbfb8aa3b, v108
	v_exp_f32_e32 v112, v112
	v_pk_mul_f32 v[170:171], v[54:55], v[118:119]
	v_add_f32_e32 v112, 1.0, v112
	v_rcp_f32_e32 v112, v112
	s_nop 0
	v_mul_f32_e32 v108, v108, v112
	v_mul_f32_e32 v112, 0x3d800000, v108
	v_cndmask_b32_e64 v108, v108, v112, s[18:19]
	v_add_f32_e32 v112, v186, v187
	v_add_f32_e32 v112, v112, v170
	v_add_f32_e32 v112, v112, v171
	v_mul_f32_e32 v170, 0xbfb8aa3b, v112
	v_exp_f32_e32 v170, v170
	v_lshlrev_b32_e32 v171, 16, v113
	v_and_b32_e32 v113, 0xffff0000, v113
	v_cvt_pk_bf16_f32 v108, v198, v108
	v_add_f32_e32 v170, 1.0, v170
	v_rcp_f32_e32 v170, v170
	s_nop 0
	v_mul_f32_e32 v112, v112, v170
	v_mul_f32_e32 v170, 0x3d800000, v112
	v_cndmask_b32_e64 v202, v112, v170, s[18:19]
	v_lshlrev_b32_e32 v170, 16, v109
	v_pk_mov_b32 v[168:169], v[168:169], v[170:171] op_sel:[1,0]
	v_add_f32_e32 v112, v166, v167
	v_pk_mul_f32 v[186:187], v[140:141], v[168:169]
	s_nop 0
	v_add_f32_e32 v112, v112, v186
	v_add_f32_e32 v112, v112, v187
	v_mul_f32_e32 v166, 0xbfb8aa3b, v112
	v_exp_f32_e32 v166, v166
	s_nop 0
	v_add_f32_e32 v166, 1.0, v166
	v_rcp_f32_e32 v166, v166
	s_nop 0
	v_mul_f32_e32 v112, v112, v166
	v_mul_f32_e32 v166, 0x3d800000, v112
	v_cndmask_b32_e64 v186, v112, v166, s[18:19]
	v_pk_mul_f32 v[166:167], v[140:141], v[170:171]
	v_add_f32_e32 v112, v184, v185
	v_add_f32_e32 v112, v112, v166
	v_add_f32_e32 v112, v112, v167
	v_mul_f32_e32 v166, 0xbfb8aa3b, v112
	v_exp_f32_e32 v166, v166
	s_nop 0
	v_add_f32_e32 v166, 1.0, v166
	v_rcp_f32_e32 v166, v166
	s_nop 0
	v_mul_f32_e32 v112, v112, v166
	v_mul_f32_e32 v166, 0x3d800000, v112
	v_cndmask_b32_e64 v184, v112, v166, s[18:19]
	v_and_b32_e32 v112, 0xffff0000, v109
	v_pk_mov_b32 v[198:199], v[120:121], v[112:113] op_sel:[1,0]
	v_pk_mul_f32 v[166:167], v[144:145], v[120:121]
	v_pk_mul_f32 v[120:121], v[56:57], v[198:199]
	v_add_f32_e32 v109, v116, v117
	v_add_f32_e32 v109, v109, v120
	v_add_f32_e32 v109, v109, v121
	v_mul_f32_e32 v116, 0xbfb8aa3b, v109
	v_exp_f32_e32 v116, v116
	v_pk_mul_f32 v[120:121], v[162:163], v[188:189]
	v_pk_mul_f32 v[188:189], v[160:161], v[182:183]
	v_add_f32_e32 v116, 1.0, v116
	v_rcp_f32_e32 v116, v116
	s_nop 0
	v_mul_f32_e32 v109, v109, v116
	v_mul_f32_e32 v116, 0x3d800000, v109
	v_cndmask_b32_e64 v109, v109, v116, s[18:19]
	v_cvt_pk_bf16_f32 v109, v186, v109
	global_store_dwordx4 v[114:115], v[106:109], off
	v_or_b32_e32 v114, 0x1800, v164
	v_mov_b32_e32 v115, v165
	v_pk_mul_f32 v[106:107], v[56:57], v[112:113]
	v_add_f32_e32 v108, v166, v167
	v_add_f32_e32 v106, v108, v106
	v_add_f32_e32 v106, v106, v107
	v_mul_f32_e32 v107, 0xbfb8aa3b, v106
	v_exp_f32_e32 v107, v107
	v_lshl_add_u64 v[114:115], v[138:139], 0, v[114:115]
	v_pk_mul_f32 v[186:187], v[154:155], v[190:191]
	v_pk_mul_f32 v[116:117], v[150:151], v[194:195]
	v_add_f32_e32 v107, 1.0, v107
	v_rcp_f32_e32 v107, v107
	s_nop 0
	v_mul_f32_e32 v106, v106, v107
	v_mul_f32_e32 v107, 0x3d800000, v106
	v_cndmask_b32_e64 v109, v106, v107, s[18:19]
	v_cvt_pk_bf16_f32 v106, v126, v196
	v_cvt_pk_bf16_f32 v107, v197, v200
	v_cvt_pk_bf16_f32 v108, v201, v202
	v_cvt_pk_bf16_f32 v109, v184, v109
	global_store_dwordx4 v[114:115], v[106:109], off
	v_or_b32_e32 v114, 0x2000, v164
	v_mov_b32_e32 v115, v165
	v_lshl_add_u64 v[166:167], v[138:139], 0, v[114:115]
	s_waitcnt vmcnt(14)
	v_lshlrev_b32_e32 v115, 16, v102
	v_lshlrev_b32_e32 v114, 16, v98
	v_pk_mul_f32 v[106:107], v[160:161], v[180:181]
	v_pk_mov_b32 v[180:181], v[182:183], v[114:115] op_sel:[1,0]
	v_add_f32_e32 v106, v106, v107
	v_pk_mul_f32 v[182:183], v[158:159], v[180:181]
	v_add_f32_e32 v126, v188, v189
	v_add_f32_e32 v106, v106, v182
	v_add_f32_e32 v106, v106, v183
	v_mul_f32_e32 v107, 0xbfb8aa3b, v106
	v_exp_f32_e32 v107, v107
	v_pk_mul_f32 v[182:183], v[162:163], v[174:175]
	v_pk_mul_f32 v[184:185], v[156:157], v[192:193]
	v_pk_mul_f32 v[108:109], v[148:149], v[172:173]
	v_add_f32_e32 v107, 1.0, v107
	v_rcp_f32_e32 v107, v107
	v_add_f32_e32 v108, v108, v109
	v_pk_mul_f32 v[172:173], v[142:143], v[168:169]
	v_pk_mul_f32 v[168:169], v[144:145], v[198:199]
	v_mul_f32_e32 v106, v106, v107
	v_mul_f32_e32 v107, 0x3d800000, v106
	v_cndmask_b32_e64 v190, v106, v107, s[18:19]
	v_pk_mul_f32 v[106:107], v[158:159], v[114:115]
	s_nop 0
	v_add_f32_e32 v106, v126, v106
	v_add_f32_e32 v106, v106, v107
	v_mul_f32_e32 v107, 0xbfb8aa3b, v106
	v_exp_f32_e32 v107, v107
	s_nop 0
	v_add_f32_e32 v107, 1.0, v107
	v_rcp_f32_e32 v107, v107
	s_nop 0
	v_mul_f32_e32 v106, v106, v107
	v_mul_f32_e32 v107, 0x3d800000, v106
	v_cndmask_b32_e64 v126, v106, v107, s[18:19]
	v_and_b32_e32 v107, 0xffff0000, v102
	v_and_b32_e32 v106, 0xffff0000, v98
	v_pk_mov_b32 v[174:175], v[174:175], v[106:107] op_sel:[1,0]
	v_add_f32_e32 v98, v120, v121
	v_pk_mul_f32 v[188:189], v[50:51], v[174:175]
	v_pk_mul_f32 v[120:121], v[50:51], v[106:107]
	v_add_f32_e32 v98, v98, v188
	v_add_f32_e32 v98, v98, v189
	v_mul_f32_e32 v102, 0xbfb8aa3b, v98
	v_exp_f32_e32 v102, v102
	s_nop 0
	v_add_f32_e32 v102, 1.0, v102
	v_rcp_f32_e32 v102, v102
	s_nop 0
	v_mul_f32_e32 v98, v98, v102
	v_mul_f32_e32 v102, 0x3d800000, v98
	v_cndmask_b32_e64 v98, v98, v102, s[18:19]
	v_add_f32_e32 v102, v182, v183
	v_add_f32_e32 v102, v102, v120
	v_add_f32_e32 v102, v102, v121
	v_mul_f32_e32 v120, 0xbfb8aa3b, v102
	v_exp_f32_e32 v120, v120
	v_lshlrev_b32_e32 v121, 16, v103
	v_pk_mul_f32 v[182:183], v[154:155], v[178:179]
	v_cvt_pk_bf16_f32 v98, v190, v98
	v_add_f32_e32 v120, 1.0, v120
	v_rcp_f32_e32 v120, v120
	v_and_b32_e32 v103, 0xffff0000, v103
	v_mul_f32_e32 v102, v102, v120
	v_mul_f32_e32 v120, 0x3d800000, v102
	v_cndmask_b32_e64 v188, v102, v120, s[18:19]
	v_lshlrev_b32_e32 v120, 16, v99
	v_pk_mov_b32 v[178:179], v[178:179], v[120:121] op_sel:[1,0]
	v_add_f32_e32 v102, v186, v187
	v_pk_mul_f32 v[190:191], v[152:153], v[178:179]
	v_pk_mul_f32 v[178:179], v[154:155], v[178:179]
	v_add_f32_e32 v102, v102, v190
	v_add_f32_e32 v102, v102, v191
	v_mul_f32_e32 v186, 0xbfb8aa3b, v102
	v_exp_f32_e32 v186, v186
	v_pk_mul_f32 v[190:191], v[156:157], v[110:111]
	v_add_f32_e32 v186, 1.0, v186
	v_rcp_f32_e32 v186, v186
	s_nop 0
	v_mul_f32_e32 v102, v102, v186
	v_mul_f32_e32 v186, 0x3d800000, v102
	v_cndmask_b32_e64 v189, v102, v186, s[18:19]
	v_pk_mul_f32 v[186:187], v[152:153], v[120:121]
	v_add_f32_e32 v102, v182, v183
	v_add_f32_e32 v102, v102, v186
	v_add_f32_e32 v102, v102, v187
	v_mul_f32_e32 v182, 0xbfb8aa3b, v102
	v_exp_f32_e32 v182, v182
	s_nop 0
	v_add_f32_e32 v182, 1.0, v182
	v_rcp_f32_e32 v182, v182
	s_nop 0
	v_mul_f32_e32 v102, v102, v182
	v_mul_f32_e32 v182, 0x3d800000, v102
	v_cndmask_b32_e64 v186, v102, v182, s[18:19]
	v_and_b32_e32 v102, 0xffff0000, v99
	v_pk_mov_b32 v[182:183], v[110:111], v[102:103] op_sel:[1,0]
	v_add_f32_e32 v99, v184, v185
	v_pk_mul_f32 v[110:111], v[52:53], v[182:183]
	v_add_f32_e32 v184, v190, v191
	v_add_f32_e32 v99, v99, v110
	v_add_f32_e32 v99, v99, v111
	v_mul_f32_e32 v110, 0xbfb8aa3b, v99
	v_exp_f32_e32 v110, v110
	s_nop 0
	v_add_f32_e32 v110, 1.0, v110
	v_rcp_f32_e32 v110, v110
	s_nop 0
	v_mul_f32_e32 v99, v99, v110
	v_mul_f32_e32 v110, 0x3d800000, v99
	v_cndmask_b32_e64 v99, v99, v110, s[18:19]
	v_pk_mul_f32 v[110:111], v[52:53], v[102:103]
	v_cvt_pk_bf16_f32 v99, v189, v99
	s_nop 0
	v_add_f32_e32 v110, v184, v110
	v_add_f32_e32 v110, v110, v111
	v_mul_f32_e32 v111, 0xbfb8aa3b, v110
	v_exp_f32_e32 v111, v111
	v_pk_mul_f32 v[184:185], v[148:149], v[176:177]
	v_add_f32_e32 v111, 1.0, v111
	v_rcp_f32_e32 v111, v111
	v_add_f32_e32 v184, v184, v185
	v_mul_f32_e32 v110, v110, v111
	v_mul_f32_e32 v111, 0x3d800000, v110
	v_cndmask_b32_e64 v187, v110, v111, s[18:19]
	v_lshlrev_b32_e32 v111, 16, v104
	v_lshlrev_b32_e32 v110, 16, v100
	v_pk_mov_b32 v[176:177], v[176:177], v[110:111] op_sel:[1,0]
	s_nop 0
	v_pk_mul_f32 v[190:191], v[146:147], v[176:177]
	v_pk_mul_f32 v[176:177], v[148:149], v[176:177]
	v_add_f32_e32 v108, v108, v190
	v_add_f32_e32 v108, v108, v191
	v_mul_f32_e32 v109, 0xbfb8aa3b, v108
	v_exp_f32_e32 v109, v109
	v_add_f32_e32 v176, v176, v177
	v_add_f32_e32 v109, 1.0, v109
	v_rcp_f32_e32 v109, v109
	s_nop 0
	v_mul_f32_e32 v108, v108, v109
	v_mul_f32_e32 v109, 0x3d800000, v108
	v_cndmask_b32_e64 v189, v108, v109, s[18:19]
	v_pk_mul_f32 v[108:109], v[146:147], v[110:111]
	s_nop 0
	v_add_f32_e32 v108, v184, v108
	v_add_f32_e32 v108, v108, v109
	v_mul_f32_e32 v109, 0xbfb8aa3b, v108
	v_exp_f32_e32 v109, v109
	v_pk_mul_f32 v[184:185], v[150:151], v[118:119]
	v_add_f32_e32 v109, 1.0, v109
	v_rcp_f32_e32 v109, v109
	s_nop 0
	v_mul_f32_e32 v108, v108, v109
	v_mul_f32_e32 v109, 0x3d800000, v108
	v_cndmask_b32_e64 v192, v108, v109, s[18:19]
	v_and_b32_e32 v109, 0xffff0000, v104
	v_and_b32_e32 v108, 0xffff0000, v100
	v_pk_mov_b32 v[118:119], v[118:119], v[108:109] op_sel:[1,0]
	v_add_f32_e32 v100, v116, v117
	v_pk_mul_f32 v[190:191], v[54:55], v[118:119]
	v_pk_mul_f32 v[116:117], v[54:55], v[108:109]
	v_add_f32_e32 v100, v100, v190
	v_add_f32_e32 v100, v100, v191
	v_mul_f32_e32 v104, 0xbfb8aa3b, v100
	v_exp_f32_e32 v104, v104
	s_nop 0
	v_add_f32_e32 v104, 1.0, v104
	v_rcp_f32_e32 v104, v104
	s_nop 0
	v_mul_f32_e32 v100, v100, v104
	v_mul_f32_e32 v104, 0x3d800000, v100
	v_cndmask_b32_e64 v100, v100, v104, s[18:19]
	v_add_f32_e32 v104, v184, v185
	v_add_f32_e32 v104, v104, v116
	v_add_f32_e32 v104, v104, v117
	v_mul_f32_e32 v116, 0xbfb8aa3b, v104
	v_exp_f32_e32 v116, v116
	v_cvt_pk_bf16_f32 v100, v189, v100
	v_lshlrev_b32_e32 v117, 16, v105
	v_pk_mul_f32 v[184:185], v[142:143], v[170:171]
	v_add_f32_e32 v116, 1.0, v116
	v_rcp_f32_e32 v116, v116
	v_and_b32_e32 v105, 0xffff0000, v105
	v_mul_f32_e32 v104, v104, v116
	v_mul_f32_e32 v116, 0x3d800000, v104
	v_cndmask_b32_e64 v189, v104, v116, s[18:19]
	v_lshlrev_b32_e32 v116, 16, v101
	v_pk_mov_b32 v[170:171], v[170:171], v[116:117] op_sel:[1,0]
	v_add_f32_e32 v104, v172, v173
	v_pk_mul_f32 v[190:191], v[140:141], v[170:171]
	s_nop 0
	v_add_f32_e32 v104, v104, v190
	v_add_f32_e32 v104, v104, v191
	v_mul_f32_e32 v172, 0xbfb8aa3b, v104
	v_exp_f32_e32 v172, v172
	s_nop 0
	v_add_f32_e32 v172, 1.0, v172
	v_rcp_f32_e32 v172, v172
	s_nop 0
	v_mul_f32_e32 v104, v104, v172
	v_mul_f32_e32 v172, 0x3d800000, v104
	v_cndmask_b32_e64 v190, v104, v172, s[18:19]
	v_pk_mul_f32 v[172:173], v[140:141], v[116:117]
	v_add_f32_e32 v104, v184, v185
	v_add_f32_e32 v104, v104, v172
	v_add_f32_e32 v104, v104, v173
	v_mul_f32_e32 v172, 0xbfb8aa3b, v104
	v_exp_f32_e32 v172, v172
	s_nop 0
	v_add_f32_e32 v172, 1.0, v172
	v_rcp_f32_e32 v172, v172
	s_nop 0
	v_mul_f32_e32 v104, v104, v172
	v_mul_f32_e32 v172, 0x3d800000, v104
	v_cndmask_b32_e64 v191, v104, v172, s[18:19]
	v_and_b32_e32 v104, 0xffff0000, v101
	v_pk_mov_b32 v[184:185], v[112:113], v[104:105] op_sel:[1,0]
	v_pk_mul_f32 v[172:173], v[144:145], v[112:113]
	v_pk_mul_f32 v[112:113], v[56:57], v[184:185]
	v_add_f32_e32 v101, v168, v169
	v_add_f32_e32 v101, v101, v112
	v_add_f32_e32 v101, v101, v113
	v_mul_f32_e32 v112, 0xbfb8aa3b, v101
	v_exp_f32_e32 v112, v112
	v_mov_b32_e32 v113, v165
	v_pk_mul_f32 v[168:169], v[142:143], v[170:171]
	v_add_f32_e32 v112, 1.0, v112
	v_rcp_f32_e32 v112, v112
	s_nop 0
	v_mul_f32_e32 v101, v101, v112
	v_mul_f32_e32 v112, 0x3d800000, v101
	v_cndmask_b32_e64 v101, v101, v112, s[18:19]
	v_cvt_pk_bf16_f32 v101, v190, v101
	global_store_dwordx4 v[166:167], v[98:101], off
	v_or_b32_e32 v112, 0x2800, v164
	v_lshl_add_u64 v[112:113], v[138:139], 0, v[112:113]
	v_pk_mul_f32 v[98:99], v[56:57], v[104:105]
	v_add_f32_e32 v100, v172, v173
	v_add_f32_e32 v98, v100, v98
	v_add_f32_e32 v98, v98, v99
	v_mul_f32_e32 v99, 0xbfb8aa3b, v98
	v_exp_f32_e32 v99, v99
	v_pk_mul_f32 v[172:173], v[150:151], v[118:119]
	v_pk_mul_f32 v[166:167], v[144:145], v[184:185]
	v_add_f32_e32 v99, 1.0, v99
	v_rcp_f32_e32 v99, v99
	s_nop 0
	v_mul_f32_e32 v98, v98, v99
	v_mul_f32_e32 v99, 0x3d800000, v98
	v_cndmask_b32_e64 v101, v98, v99, s[18:19]
	v_cvt_pk_bf16_f32 v98, v126, v188
	v_cvt_pk_bf16_f32 v99, v186, v187
	v_cvt_pk_bf16_f32 v100, v192, v189
	v_cvt_pk_bf16_f32 v101, v191, v101
	global_store_dwordx4 v[112:113], v[98:101], off
	v_pk_mul_f32 v[112:113], v[156:157], v[182:183]
	s_nop 0
	v_or_b32_e32 v100, 0x3000, v164
	v_mov_b32_e32 v101, v165
	v_lshl_add_u64 v[118:119], v[138:139], 0, v[100:101]
	s_waitcnt vmcnt(14)
	v_lshlrev_b32_e32 v101, 16, v94
	v_lshlrev_b32_e32 v100, 16, v90
	v_pk_mul_f32 v[98:99], v[160:161], v[180:181]
	v_pk_mov_b32 v[170:171], v[114:115], v[100:101] op_sel:[1,0]
	v_pk_mul_f32 v[180:181], v[162:163], v[174:175]
	v_pk_mul_f32 v[174:175], v[160:161], v[114:115]
	v_pk_mul_f32 v[114:115], v[158:159], v[170:171]
	v_add_f32_e32 v98, v98, v99
	v_add_f32_e32 v98, v98, v114
	v_add_f32_e32 v98, v98, v115
	v_mul_f32_e32 v99, 0xbfb8aa3b, v98
	v_exp_f32_e32 v99, v99
	v_add_f32_e32 v114, v174, v175
	v_add_f32_e32 v99, 1.0, v99
	v_rcp_f32_e32 v99, v99
	s_nop 0
	v_mul_f32_e32 v98, v98, v99
	v_mul_f32_e32 v99, 0x3d800000, v98
	v_cndmask_b32_e64 v182, v98, v99, s[18:19]
	v_pk_mul_f32 v[98:99], v[158:159], v[100:101]
	s_nop 0
	v_add_f32_e32 v98, v114, v98
	v_add_f32_e32 v98, v98, v99
	v_mul_f32_e32 v99, 0xbfb8aa3b, v98
	v_exp_f32_e32 v99, v99
	v_pk_mul_f32 v[114:115], v[162:163], v[106:107]
	v_add_f32_e32 v99, 1.0, v99
	v_rcp_f32_e32 v99, v99
	s_nop 0
	v_mul_f32_e32 v98, v98, v99
	v_mul_f32_e32 v99, 0x3d800000, v98
	v_cndmask_b32_e64 v126, v98, v99, s[18:19]
	v_and_b32_e32 v99, 0xffff0000, v94
	v_and_b32_e32 v98, 0xffff0000, v90
	v_pk_mov_b32 v[174:175], v[106:107], v[98:99] op_sel:[1,0]
	v_add_f32_e32 v90, v180, v181
	v_pk_mul_f32 v[106:107], v[50:51], v[174:175]
	s_nop 0
	v_add_f32_e32 v90, v90, v106
	v_add_f32_e32 v90, v90, v107
	v_mul_f32_e32 v94, 0xbfb8aa3b, v90
	v_exp_f32_e32 v94, v94
	v_pk_mul_f32 v[106:107], v[50:51], v[98:99]
	v_add_f32_e32 v94, 1.0, v94
	v_rcp_f32_e32 v94, v94
	s_nop 0
	v_mul_f32_e32 v90, v90, v94
	v_mul_f32_e32 v94, 0x3d800000, v90
	v_cndmask_b32_e64 v90, v90, v94, s[18:19]
	v_add_f32_e32 v94, v114, v115
	v_add_f32_e32 v94, v94, v106
	v_add_f32_e32 v94, v94, v107
	v_mul_f32_e32 v106, 0xbfb8aa3b, v94
	v_exp_f32_e32 v106, v106
	v_lshlrev_b32_e32 v115, 16, v95
	v_lshlrev_b32_e32 v114, 16, v91
	v_cvt_pk_bf16_f32 v90, v182, v90
	v_add_f32_e32 v106, 1.0, v106
	v_rcp_f32_e32 v106, v106
	v_and_b32_e32 v95, 0xffff0000, v95
	v_mul_f32_e32 v94, v94, v106
	v_mul_f32_e32 v106, 0x3d800000, v94
	v_cndmask_b32_e64 v180, v94, v106, s[18:19]
	v_pk_mul_f32 v[106:107], v[154:155], v[120:121]
	v_pk_mov_b32 v[120:121], v[120:121], v[114:115] op_sel:[1,0]
	v_add_f32_e32 v94, v178, v179
	v_pk_mul_f32 v[182:183], v[152:153], v[120:121]
	s_nop 0
	v_add_f32_e32 v94, v94, v182
	v_add_f32_e32 v94, v94, v183
	v_mul_f32_e32 v178, 0xbfb8aa3b, v94
	v_exp_f32_e32 v178, v178
	s_nop 0
	v_add_f32_e32 v178, 1.0, v178
	v_rcp_f32_e32 v178, v178
	s_nop 0
	v_mul_f32_e32 v94, v94, v178
	v_mul_f32_e32 v178, 0x3d800000, v94
	v_cndmask_b32_e64 v182, v94, v178, s[18:19]
	v_pk_mul_f32 v[178:179], v[152:153], v[114:115]
	v_add_f32_e32 v94, v106, v107
	v_add_f32_e32 v94, v94, v178
	v_add_f32_e32 v94, v94, v179
	v_mul_f32_e32 v106, 0xbfb8aa3b, v94
	v_exp_f32_e32 v106, v106
	s_nop 0
	v_add_f32_e32 v106, 1.0, v106
	v_rcp_f32_e32 v106, v106
	s_nop 0
	v_mul_f32_e32 v94, v94, v106
	v_mul_f32_e32 v106, 0x3d800000, v94
	v_cndmask_b32_e64 v181, v94, v106, s[18:19]
	v_and_b32_e32 v94, 0xffff0000, v91
	v_pk_mul_f32 v[106:107], v[156:157], v[102:103]
	v_pk_mov_b32 v[102:103], v[102:103], v[94:95] op_sel:[1,0]
	v_add_f32_e32 v91, v112, v113
	v_pk_mul_f32 v[178:179], v[52:53], v[102:103]
	v_add_f32_e32 v106, v106, v107
	v_add_f32_e32 v91, v91, v178
	v_add_f32_e32 v91, v91, v179
	v_mul_f32_e32 v112, 0xbfb8aa3b, v91
	v_exp_f32_e32 v112, v112
	s_nop 0
	v_add_f32_e32 v112, 1.0, v112
	v_rcp_f32_e32 v112, v112
	s_nop 0
	v_mul_f32_e32 v91, v91, v112
	v_mul_f32_e32 v112, 0x3d800000, v91
	v_cndmask_b32_e64 v91, v91, v112, s[18:19]
	v_pk_mul_f32 v[112:113], v[52:53], v[94:95]
	v_cvt_pk_bf16_f32 v91, v182, v91
	s_nop 0
	v_add_f32_e32 v106, v106, v112
	v_add_f32_e32 v106, v106, v113
	v_mul_f32_e32 v107, 0xbfb8aa3b, v106
	v_exp_f32_e32 v107, v107
	v_lshlrev_b32_e32 v113, 16, v96
	v_lshlrev_b32_e32 v112, 16, v92
	v_pk_mov_b32 v[178:179], v[110:111], v[112:113] op_sel:[1,0]
	v_add_f32_e32 v107, 1.0, v107
	v_rcp_f32_e32 v107, v107
	s_nop 0
	v_mul_f32_e32 v106, v106, v107
	v_mul_f32_e32 v107, 0x3d800000, v106
	v_cndmask_b32_e64 v182, v106, v107, s[18:19]
	v_pk_mul_f32 v[106:107], v[148:149], v[110:111]
	v_pk_mul_f32 v[110:111], v[146:147], v[178:179]
	v_add_f32_e32 v106, v106, v107
	v_add_f32_e32 v110, v176, v110
	v_add_f32_e32 v110, v110, v111
	v_mul_f32_e32 v111, 0xbfb8aa3b, v110
	v_exp_f32_e32 v111, v111
	s_nop 0
	v_add_f32_e32 v111, 1.0, v111
	v_rcp_f32_e32 v111, v111
	s_nop 0
	v_mul_f32_e32 v110, v110, v111
	v_mul_f32_e32 v111, 0x3d800000, v110
	v_cndmask_b32_e64 v183, v110, v111, s[18:19]
	v_pk_mul_f32 v[110:111], v[146:147], v[112:113]
	s_nop 0
	v_add_f32_e32 v106, v106, v110
	v_add_f32_e32 v106, v106, v111
	v_mul_f32_e32 v107, 0xbfb8aa3b, v106
	v_exp_f32_e32 v107, v107
	v_pk_mul_f32 v[110:111], v[150:151], v[108:109]
	v_add_f32_e32 v107, 1.0, v107
	v_rcp_f32_e32 v107, v107
	s_nop 0
	v_mul_f32_e32 v106, v106, v107
	v_mul_f32_e32 v107, 0x3d800000, v106
	v_cndmask_b32_e64 v184, v106, v107, s[18:19]
	v_and_b32_e32 v107, 0xffff0000, v96
	v_and_b32_e32 v106, 0xffff0000, v92
	v_pk_mov_b32 v[176:177], v[108:109], v[106:107] op_sel:[1,0]
	v_add_f32_e32 v92, v172, v173
	v_pk_mul_f32 v[108:109], v[54:55], v[176:177]
	s_nop 0
	v_add_f32_e32 v92, v92, v108
	v_add_f32_e32 v92, v92, v109
	v_mul_f32_e32 v96, 0xbfb8aa3b, v92
	v_exp_f32_e32 v96, v96
	v_pk_mul_f32 v[108:109], v[54:55], v[106:107]
	v_add_f32_e32 v96, 1.0, v96
	v_rcp_f32_e32 v96, v96
	s_nop 0
	v_mul_f32_e32 v92, v92, v96
	v_mul_f32_e32 v96, 0x3d800000, v92
	v_cndmask_b32_e64 v92, v92, v96, s[18:19]
	v_add_f32_e32 v96, v110, v111
	v_add_f32_e32 v96, v96, v108
	v_add_f32_e32 v96, v96, v109
	v_mul_f32_e32 v108, 0xbfb8aa3b, v96
	v_exp_f32_e32 v108, v108
	v_lshlrev_b32_e32 v111, 16, v97
	v_lshlrev_b32_e32 v110, 16, v93
	v_cvt_pk_bf16_f32 v92, v183, v92
	v_add_f32_e32 v108, 1.0, v108
	v_rcp_f32_e32 v108, v108
	s_nop 0
	v_mul_f32_e32 v96, v96, v108
	v_mul_f32_e32 v108, 0x3d800000, v96
	v_cndmask_b32_e64 v183, v96, v108, s[18:19]
	v_pk_mul_f32 v[108:109], v[142:143], v[116:117]
	v_pk_mov_b32 v[116:117], v[116:117], v[110:111] op_sel:[1,0]
	v_add_f32_e32 v96, v168, v169
	v_pk_mul_f32 v[172:173], v[140:141], v[116:117]
	s_nop 0
	v_add_f32_e32 v96, v96, v172
	v_add_f32_e32 v96, v96, v173
	v_mul_f32_e32 v168, 0xbfb8aa3b, v96
	v_exp_f32_e32 v168, v168
	s_nop 0
	v_add_f32_e32 v168, 1.0, v168
	v_rcp_f32_e32 v168, v168
	s_nop 0
	v_mul_f32_e32 v96, v96, v168
	v_mul_f32_e32 v168, 0x3d800000, v96
	v_cndmask_b32_e64 v172, v96, v168, s[18:19]
	v_pk_mul_f32 v[168:169], v[140:141], v[110:111]
	v_add_f32_e32 v96, v108, v109
	v_add_f32_e32 v96, v96, v168
	v_add_f32_e32 v96, v96, v169
	v_mul_f32_e32 v108, 0xbfb8aa3b, v96
	v_exp_f32_e32 v108, v108
	v_and_b32_e32 v109, 0xffff0000, v97
	v_pk_mul_f32 v[168:169], v[144:145], v[104:105]
	v_add_f32_e32 v108, 1.0, v108
	v_rcp_f32_e32 v108, v108
	s_nop 0
	v_mul_f32_e32 v96, v96, v108
	v_mul_f32_e32 v108, 0x3d800000, v96
	v_cndmask_b32_e64 v173, v96, v108, s[18:19]
	v_and_b32_e32 v108, 0xffff0000, v93
	v_pk_mov_b32 v[104:105], v[104:105], v[108:109] op_sel:[1,0]
	v_add_f32_e32 v93, v166, v167
	v_pk_mul_f32 v[96:97], v[56:57], v[104:105]
	v_pk_mul_f32 v[166:167], v[160:161], v[170:171]
	v_add_f32_e32 v93, v93, v96
	v_add_f32_e32 v93, v93, v97
	v_mul_f32_e32 v96, 0xbfb8aa3b, v93
	v_exp_f32_e32 v96, v96
	v_mov_b32_e32 v97, v165
	v_pk_mul_f32 v[170:171], v[162:163], v[174:175]
	v_add_f32_e32 v96, 1.0, v96
	v_rcp_f32_e32 v96, v96
	s_nop 0
	v_mul_f32_e32 v93, v93, v96
	v_mul_f32_e32 v96, 0x3d800000, v93
	v_cndmask_b32_e64 v93, v93, v96, s[18:19]
	v_cvt_pk_bf16_f32 v93, v172, v93
	global_store_dwordx4 v[118:119], v[90:93], off
	v_or_b32_e32 v96, 0x3800, v164
	v_lshl_add_u64 v[96:97], v[138:139], 0, v[96:97]
	v_pk_mul_f32 v[90:91], v[56:57], v[108:109]
	v_add_f32_e32 v92, v168, v169
	v_add_f32_e32 v90, v92, v90
	v_add_f32_e32 v90, v90, v91
	v_mul_f32_e32 v91, 0xbfb8aa3b, v90
	v_exp_f32_e32 v91, v91
	v_pk_mul_f32 v[168:169], v[156:157], v[102:103]
	v_or_b32_e32 v102, 0x4000, v164
	v_mov_b32_e32 v103, v165
	v_add_f32_e32 v91, 1.0, v91
	v_rcp_f32_e32 v91, v91
	v_pk_mul_f32 v[118:119], v[142:143], v[116:117]
	v_pk_mul_f32 v[116:117], v[144:145], v[104:105]
	v_lshl_add_u64 v[104:105], v[138:139], 0, v[102:103]
	v_mul_f32_e32 v90, v90, v91
	v_mul_f32_e32 v91, 0x3d800000, v90
	v_cndmask_b32_e64 v93, v90, v91, s[18:19]
	s_waitcnt vmcnt(13)
	v_lshlrev_b32_e32 v103, 16, v86
	v_lshlrev_b32_e32 v102, 16, v82
	v_cvt_pk_bf16_f32 v90, v126, v180
	v_cvt_pk_bf16_f32 v91, v181, v182
	v_cvt_pk_bf16_f32 v92, v184, v183
	v_cvt_pk_bf16_f32 v93, v173, v93
	global_store_dwordx4 v[96:97], v[90:93], off
	v_pk_mul_f32 v[96:97], v[154:155], v[120:121]
	v_pk_mov_b32 v[120:121], v[100:101], v[102:103] op_sel:[1,0]
	v_pk_mul_f32 v[172:173], v[160:161], v[100:101]
	v_pk_mul_f32 v[100:101], v[158:159], v[120:121]
	v_add_f32_e32 v126, v166, v167
	v_add_f32_e32 v100, v126, v100
	v_add_f32_e32 v100, v100, v101
	v_mul_f32_e32 v101, 0xbfb8aa3b, v100
	v_exp_f32_e32 v101, v101
	v_add_f32_e32 v126, v172, v173
	v_pk_mul_f32 v[172:173], v[162:163], v[98:99]
	v_pk_mul_f32 v[90:91], v[150:151], v[176:177]
	v_add_f32_e32 v101, 1.0, v101
	v_rcp_f32_e32 v101, v101
	v_pk_mul_f32 v[92:93], v[148:149], v[178:179]
	s_waitcnt vmcnt(9)
	v_lshlrev_b32_e32 v181, 16, v66
	v_add_f32_e32 v92, v92, v93
	v_mul_f32_e32 v100, v100, v101
	v_mul_f32_e32 v101, 0x3d800000, v100
	v_cndmask_b32_e64 v174, v100, v101, s[18:19]
	v_pk_mul_f32 v[100:101], v[158:159], v[102:103]
	v_lshlrev_b32_e32 v180, 16, v62
	v_add_f32_e32 v100, v126, v100
	v_add_f32_e32 v100, v100, v101
	v_mul_f32_e32 v101, 0xbfb8aa3b, v100
	v_exp_f32_e32 v101, v101
	v_and_b32_e32 v179, 0xffff0000, v66
	v_and_b32_e32 v178, 0xffff0000, v62
	v_add_f32_e32 v101, 1.0, v101
	v_rcp_f32_e32 v101, v101
	s_nop 0
	v_mul_f32_e32 v100, v100, v101
	v_mul_f32_e32 v101, 0x3d800000, v100
	v_cndmask_b32_e64 v126, v100, v101, s[18:19]
	v_and_b32_e32 v101, 0xffff0000, v86
	v_and_b32_e32 v100, 0xffff0000, v82
	v_pk_mov_b32 v[166:167], v[98:99], v[100:101] op_sel:[1,0]
	v_add_f32_e32 v82, v170, v171
	v_pk_mul_f32 v[98:99], v[50:51], v[166:167]
	v_pk_mul_f32 v[170:171], v[154:155], v[114:115]
	v_add_f32_e32 v82, v82, v98
	v_add_f32_e32 v82, v82, v99
	v_mul_f32_e32 v86, 0xbfb8aa3b, v82
	v_exp_f32_e32 v86, v86
	v_pk_mul_f32 v[98:99], v[50:51], v[100:101]
	v_add_f32_e32 v86, 1.0, v86
	v_rcp_f32_e32 v86, v86
	s_nop 0
	v_mul_f32_e32 v82, v82, v86
	v_mul_f32_e32 v86, 0x3d800000, v82
	v_cndmask_b32_e64 v82, v82, v86, s[18:19]
	v_add_f32_e32 v86, v172, v173
	v_add_f32_e32 v86, v86, v98
	v_add_f32_e32 v86, v86, v99
	v_mul_f32_e32 v98, 0xbfb8aa3b, v86
	v_exp_f32_e32 v98, v98
	v_lshlrev_b32_e32 v99, 16, v87
	v_cvt_pk_bf16_f32 v82, v174, v82
	v_add_f32_e32 v98, 1.0, v98
	v_rcp_f32_e32 v98, v98
	s_nop 0
	v_mul_f32_e32 v86, v86, v98
	v_mul_f32_e32 v98, 0x3d800000, v86
	v_cndmask_b32_e64 v172, v86, v98, s[18:19]
	v_lshlrev_b32_e32 v98, 16, v83
	v_pk_mov_b32 v[114:115], v[114:115], v[98:99] op_sel:[1,0]
	v_add_f32_e32 v86, v96, v97
	v_pk_mul_f32 v[174:175], v[152:153], v[114:115]
	s_nop 0
	v_add_f32_e32 v86, v86, v174
	v_add_f32_e32 v86, v86, v175
	v_mul_f32_e32 v96, 0xbfb8aa3b, v86
	v_exp_f32_e32 v96, v96
	v_pk_mul_f32 v[174:175], v[156:157], v[94:95]
	v_add_f32_e32 v96, 1.0, v96
	v_rcp_f32_e32 v96, v96
	s_nop 0
	v_mul_f32_e32 v86, v86, v96
	v_mul_f32_e32 v96, 0x3d800000, v86
	v_cndmask_b32_e64 v176, v86, v96, s[18:19]
	v_pk_mul_f32 v[96:97], v[152:153], v[98:99]
	v_add_f32_e32 v86, v170, v171
	v_add_f32_e32 v86, v86, v96
	v_add_f32_e32 v86, v86, v97
	v_mul_f32_e32 v96, 0xbfb8aa3b, v86
	v_exp_f32_e32 v96, v96
	v_and_b32_e32 v97, 0xffff0000, v87
	v_add_f32_e32 v96, 1.0, v96
	v_rcp_f32_e32 v96, v96
	s_nop 0
	v_mul_f32_e32 v86, v86, v96
	v_mul_f32_e32 v96, 0x3d800000, v86
	v_cndmask_b32_e64 v173, v86, v96, s[18:19]
	v_and_b32_e32 v96, 0xffff0000, v83
	v_pk_mov_b32 v[170:171], v[94:95], v[96:97] op_sel:[1,0]
	v_add_f32_e32 v83, v168, v169
	v_pk_mul_f32 v[86:87], v[52:53], v[170:171]
	v_add_f32_e32 v94, v174, v175
	v_add_f32_e32 v83, v83, v86
	v_add_f32_e32 v83, v83, v87
	v_mul_f32_e32 v86, 0xbfb8aa3b, v83
	v_exp_f32_e32 v86, v86
	v_lshlrev_b32_e32 v95, 16, v88
	v_add_f32_e32 v86, 1.0, v86
	v_rcp_f32_e32 v86, v86
	s_nop 0
	v_mul_f32_e32 v83, v83, v86
	v_mul_f32_e32 v86, 0x3d800000, v83
	v_cndmask_b32_e64 v83, v83, v86, s[18:19]
	v_pk_mul_f32 v[86:87], v[52:53], v[96:97]
	v_cvt_pk_bf16_f32 v83, v176, v83
	s_nop 0
	v_add_f32_e32 v86, v94, v86
	v_add_f32_e32 v86, v86, v87
	v_mul_f32_e32 v87, 0xbfb8aa3b, v86
	v_exp_f32_e32 v87, v87
	v_lshlrev_b32_e32 v94, 16, v84
	v_pk_mov_b32 v[168:169], v[112:113], v[94:95] op_sel:[1,0]
	v_add_f32_e32 v87, 1.0, v87
	v_rcp_f32_e32 v87, v87
	s_nop 0
	v_mul_f32_e32 v86, v86, v87
	v_mul_f32_e32 v87, 0x3d800000, v86
	v_cndmask_b32_e64 v176, v86, v87, s[18:19]
	v_pk_mul_f32 v[86:87], v[148:149], v[112:113]
	v_pk_mul_f32 v[112:113], v[146:147], v[168:169]
	v_add_f32_e32 v86, v86, v87
	v_add_f32_e32 v92, v92, v112
	v_add_f32_e32 v92, v92, v113
	v_mul_f32_e32 v93, 0xbfb8aa3b, v92
	v_exp_f32_e32 v93, v93
	s_nop 0
	v_add_f32_e32 v93, 1.0, v93
	v_rcp_f32_e32 v93, v93
	s_nop 0
	v_mul_f32_e32 v92, v92, v93
	v_mul_f32_e32 v93, 0x3d800000, v92
	v_cndmask_b32_e64 v174, v92, v93, s[18:19]
	v_pk_mul_f32 v[92:93], v[146:147], v[94:95]
	s_nop 0
	v_add_f32_e32 v86, v86, v92
	v_add_f32_e32 v86, v86, v93
	v_mul_f32_e32 v87, 0xbfb8aa3b, v86
	v_exp_f32_e32 v87, v87
	v_and_b32_e32 v93, 0xffff0000, v88
	v_and_b32_e32 v92, 0xffff0000, v84
	v_add_f32_e32 v84, v90, v91
	v_add_f32_e32 v87, 1.0, v87
	v_rcp_f32_e32 v87, v87
	v_pk_mul_f32 v[90:91], v[54:55], v[92:93]
	v_mul_f32_e32 v86, v86, v87
	v_mul_f32_e32 v87, 0x3d800000, v86
	v_cndmask_b32_e64 v177, v86, v87, s[18:19]
	v_pk_mul_f32 v[86:87], v[150:151], v[106:107]
	v_pk_mov_b32 v[106:107], v[106:107], v[92:93] op_sel:[1,0]
	v_add_f32_e32 v86, v86, v87
	v_pk_mul_f32 v[112:113], v[54:55], v[106:107]
	v_add_f32_e32 v86, v86, v90
	v_add_f32_e32 v84, v84, v112
	v_add_f32_e32 v84, v84, v113
	v_mul_f32_e32 v88, 0xbfb8aa3b, v84
	v_exp_f32_e32 v88, v88
	v_add_f32_e32 v86, v86, v91
	v_mul_f32_e32 v87, 0xbfb8aa3b, v86
	v_exp_f32_e32 v87, v87
	v_add_f32_e32 v88, 1.0, v88
	v_rcp_f32_e32 v88, v88
	v_lshlrev_b32_e32 v91, 16, v89
	v_add_f32_e32 v87, 1.0, v87
	v_rcp_f32_e32 v87, v87
	v_mul_f32_e32 v84, v84, v88
	v_mul_f32_e32 v88, 0x3d800000, v84
	v_cndmask_b32_e64 v84, v84, v88, s[18:19]
	v_mul_f32_e32 v86, v86, v87
	v_lshlrev_b32_e32 v90, 16, v85
	v_cvt_pk_bf16_f32 v84, v174, v84
	v_mul_f32_e32 v87, 0x3d800000, v86
	v_pk_mov_b32 v[174:175], v[110:111], v[90:91] op_sel:[1,0]
	v_cndmask_b32_e64 v112, v86, v87, s[18:19]
	v_pk_mul_f32 v[86:87], v[142:143], v[110:111]
	v_pk_mul_f32 v[110:111], v[140:141], v[174:175]
	v_add_f32_e32 v88, v118, v119
	v_add_f32_e32 v88, v88, v110
	v_add_f32_e32 v88, v88, v111
	v_mul_f32_e32 v110, 0xbfb8aa3b, v88
	v_exp_f32_e32 v110, v110
	v_add_f32_e32 v86, v86, v87
	v_pk_mul_f32 v[106:107], v[150:151], v[106:107]
	v_add_f32_e32 v110, 1.0, v110
	v_rcp_f32_e32 v110, v110
	s_nop 0
	v_mul_f32_e32 v88, v88, v110
	v_mul_f32_e32 v110, 0x3d800000, v88
	v_cndmask_b32_e64 v113, v88, v110, s[18:19]
	v_pk_mul_f32 v[110:111], v[140:141], v[90:91]
	s_nop 0
	v_add_f32_e32 v86, v86, v110
	v_add_f32_e32 v86, v86, v111
	v_mul_f32_e32 v87, 0xbfb8aa3b, v86
	v_exp_f32_e32 v87, v87
	v_pk_mul_f32 v[110:111], v[144:145], v[108:109]
	v_add_f32_e32 v87, 1.0, v87
	v_rcp_f32_e32 v87, v87
	s_nop 0
	v_mul_f32_e32 v86, v86, v87
	v_mul_f32_e32 v87, 0x3d800000, v86
	v_cndmask_b32_e64 v118, v86, v87, s[18:19]
	v_and_b32_e32 v87, 0xffff0000, v89
	v_and_b32_e32 v86, 0xffff0000, v85
	v_pk_mov_b32 v[88:89], v[108:109], v[86:87] op_sel:[1,0]
	v_add_f32_e32 v85, v116, v117
	v_pk_mul_f32 v[108:109], v[56:57], v[88:89]
	v_pk_mul_f32 v[116:117], v[160:161], v[120:121]
	v_add_f32_e32 v85, v85, v108
	v_add_f32_e32 v85, v85, v109
	v_mul_f32_e32 v108, 0xbfb8aa3b, v85
	v_exp_f32_e32 v108, v108
	v_add_f32_e32 v116, v116, v117
	v_and_b32_e32 v117, 0xffff0000, v78
	v_pk_mul_f32 v[120:121], v[162:163], v[166:167]
	v_add_f32_e32 v108, 1.0, v108
	v_rcp_f32_e32 v108, v108
	v_pk_mul_f32 v[166:167], v[162:163], v[100:101]
	v_pk_mul_f32 v[88:89], v[144:145], v[88:89]
	v_mul_f32_e32 v85, v85, v108
	v_mul_f32_e32 v108, 0x3d800000, v85
	v_cndmask_b32_e64 v85, v85, v108, s[18:19]
	v_cvt_pk_bf16_f32 v85, v113, v85
	global_store_dwordx4 v[104:105], v[82:85], off
	v_or_b32_e32 v104, 0x4800, v164
	v_mov_b32_e32 v105, v165
	v_pk_mul_f32 v[82:83], v[56:57], v[86:87]
	v_add_f32_e32 v84, v110, v111
	v_add_f32_e32 v82, v84, v82
	v_add_f32_e32 v82, v82, v83
	v_mul_f32_e32 v83, 0xbfb8aa3b, v82
	v_exp_f32_e32 v83, v83
	v_lshl_add_u64 v[104:105], v[138:139], 0, v[104:105]
	v_pk_mul_f32 v[108:109], v[148:149], v[168:169]
	v_pk_mul_f32 v[168:169], v[154:155], v[98:99]
	v_add_f32_e32 v83, 1.0, v83
	v_rcp_f32_e32 v83, v83
	v_pk_mul_f32 v[110:111], v[156:157], v[170:171]
	v_and_b32_e32 v171, 0xffff0000, v80
	v_and_b32_e32 v170, 0xffff0000, v76
	v_mul_f32_e32 v82, v82, v83
	v_mul_f32_e32 v83, 0x3d800000, v82
	v_cndmask_b32_e64 v85, v82, v83, s[18:19]
	v_cvt_pk_bf16_f32 v82, v126, v172
	v_cvt_pk_bf16_f32 v83, v173, v176
	v_cvt_pk_bf16_f32 v84, v177, v112
	v_cvt_pk_bf16_f32 v85, v118, v85
	global_store_dwordx4 v[104:105], v[82:85], off
	v_pk_mul_f32 v[112:113], v[154:155], v[114:115]
	v_pk_mul_f32 v[118:119], v[160:161], v[102:103]
	v_or_b32_e32 v82, 0x5000, v164
	v_mov_b32_e32 v83, v165
	v_lshl_add_u64 v[84:85], v[138:139], 0, v[82:83]
	v_lshlrev_b32_e32 v82, 16, v74
	v_lshlrev_b32_e32 v83, 16, v78
	v_pk_mov_b32 v[114:115], v[102:103], v[82:83] op_sel:[1,0]
	v_lshlrev_b32_e32 v172, 16, v77
	v_pk_mul_f32 v[102:103], v[158:159], v[114:115]
	v_lshlrev_b32_e32 v173, 16, v81
	v_add_f32_e32 v102, v116, v102
	v_add_f32_e32 v102, v102, v103
	v_mul_f32_e32 v103, 0xbfb8aa3b, v102
	v_exp_f32_e32 v103, v103
	v_add_f32_e32 v116, v118, v119
	v_pk_mul_f32 v[104:105], v[142:143], v[174:175]
	v_and_b32_e32 v175, 0xffff0000, v81
	v_add_f32_e32 v103, 1.0, v103
	v_rcp_f32_e32 v103, v103
	v_and_b32_e32 v174, 0xffff0000, v77
	v_add_f32_e32 v77, v88, v89
	v_lshlrev_b32_e32 v177, 16, v67
	v_mul_f32_e32 v102, v102, v103
	v_mul_f32_e32 v103, 0x3d800000, v102
	v_cndmask_b32_e64 v126, v102, v103, s[18:19]
	v_pk_mul_f32 v[102:103], v[158:159], v[82:83]
	v_lshlrev_b32_e32 v176, 16, v63
	v_add_f32_e32 v102, v116, v102
	v_and_b32_e32 v116, 0xffff0000, v74
	v_pk_mov_b32 v[118:119], v[100:101], v[116:117] op_sel:[1,0]
	v_add_f32_e32 v74, v120, v121
	v_pk_mul_f32 v[100:101], v[50:51], v[118:119]
	v_lshlrev_b32_e32 v120, 16, v75
	v_add_f32_e32 v74, v74, v100
	v_add_f32_e32 v74, v74, v101
	v_mul_f32_e32 v78, 0xbfb8aa3b, v74
	v_exp_f32_e32 v78, v78
	v_pk_mul_f32 v[100:101], v[50:51], v[116:117]
	v_lshlrev_b32_e32 v121, 16, v79
	v_and_b32_e32 v79, 0xffff0000, v79
	v_add_f32_e32 v78, 1.0, v78
	v_rcp_f32_e32 v78, v78
	v_add_f32_e32 v102, v102, v103
	v_mul_f32_e32 v103, 0xbfb8aa3b, v102
	v_exp_f32_e32 v103, v103
	v_mul_f32_e32 v74, v74, v78
	v_mul_f32_e32 v78, 0x3d800000, v74
	v_cndmask_b32_e64 v74, v74, v78, s[18:19]
	v_add_f32_e32 v78, v166, v167
	v_add_f32_e32 v78, v78, v100
	v_add_f32_e32 v78, v78, v101
	v_mul_f32_e32 v100, 0xbfb8aa3b, v78
	v_exp_f32_e32 v100, v100
	v_pk_mov_b32 v[166:167], v[98:99], v[120:121] op_sel:[1,0]
	v_cvt_pk_bf16_f32 v74, v126, v74
	v_add_f32_e32 v103, 1.0, v103
	v_add_f32_e32 v100, 1.0, v100
	v_rcp_f32_e32 v100, v100
	v_pk_mul_f32 v[98:99], v[152:153], v[166:167]
	v_rcp_f32_e32 v103, v103
	v_pk_mul_f32 v[88:89], v[154:155], v[120:121]
	v_mul_f32_e32 v78, v78, v100
	v_mul_f32_e32 v100, 0x3d800000, v78
	v_cndmask_b32_e64 v100, v78, v100, s[18:19]
	v_add_f32_e32 v78, v112, v113
	v_add_f32_e32 v78, v78, v98
	v_add_f32_e32 v78, v78, v99
	v_mul_f32_e32 v98, 0xbfb8aa3b, v78
	v_exp_f32_e32 v98, v98
	v_pk_mul_f32 v[112:113], v[156:157], v[96:97]
	v_mul_f32_e32 v102, v102, v103
	v_mul_f32_e32 v103, 0x3d800000, v102
	v_add_f32_e32 v98, 1.0, v98
	v_rcp_f32_e32 v98, v98
	v_cndmask_b32_e64 v102, v102, v103, s[18:19]
	v_mul_f32_e32 v78, v78, v98
	v_mul_f32_e32 v98, 0x3d800000, v78
	v_cndmask_b32_e64 v101, v78, v98, s[18:19]
	v_pk_mul_f32 v[98:99], v[152:153], v[120:121]
	v_add_f32_e32 v78, v168, v169
	v_add_f32_e32 v78, v78, v98
	v_add_f32_e32 v78, v78, v99
	v_mul_f32_e32 v98, 0xbfb8aa3b, v78
	v_exp_f32_e32 v98, v98
	s_nop 0
	v_add_f32_e32 v98, 1.0, v98
	v_rcp_f32_e32 v98, v98
	s_nop 0
	v_mul_f32_e32 v78, v78, v98
	v_mul_f32_e32 v98, 0x3d800000, v78
	v_cndmask_b32_e64 v98, v78, v98, s[18:19]
	v_and_b32_e32 v78, 0xffff0000, v75
	v_pk_mov_b32 v[96:97], v[96:97], v[78:79] op_sel:[1,0]
	v_add_f32_e32 v75, v110, v111
	v_pk_mul_f32 v[168:169], v[52:53], v[96:97]
	v_pk_mul_f32 v[110:111], v[52:53], v[78:79]
	v_add_f32_e32 v75, v75, v168
	v_add_f32_e32 v75, v75, v169
	v_mul_f32_e32 v99, 0xbfb8aa3b, v75
	v_exp_f32_e32 v99, v99
	v_lshlrev_b32_e32 v168, 16, v76
	v_lshlrev_b32_e32 v169, 16, v80
	v_add_f32_e32 v76, v106, v107
	v_add_f32_e32 v99, 1.0, v99
	v_rcp_f32_e32 v99, v99
	v_pk_mul_f32 v[106:107], v[54:55], v[170:171]
	v_mul_f32_e32 v75, v75, v99
	v_mul_f32_e32 v99, 0x3d800000, v75
	v_cndmask_b32_e64 v75, v75, v99, s[18:19]
	v_add_f32_e32 v99, v112, v113
	v_add_f32_e32 v99, v99, v110
	v_add_f32_e32 v99, v99, v111
	v_cvt_pk_bf16_f32 v75, v101, v75
	v_mul_f32_e32 v101, 0xbfb8aa3b, v99
	v_exp_f32_e32 v101, v101
	v_pk_mul_f32 v[110:111], v[148:149], v[94:95]
	v_pk_mov_b32 v[94:95], v[94:95], v[168:169] op_sel:[1,0]
	v_add_f32_e32 v101, 1.0, v101
	v_rcp_f32_e32 v101, v101
	v_pk_mul_f32 v[112:113], v[146:147], v[94:95]
	v_mul_f32_e32 v99, v99, v101
	v_mul_f32_e32 v101, 0x3d800000, v99
	v_cndmask_b32_e64 v99, v99, v101, s[18:19]
	v_add_f32_e32 v101, v108, v109
	v_add_f32_e32 v101, v101, v112
	v_add_f32_e32 v101, v101, v113
	v_mul_f32_e32 v103, 0xbfb8aa3b, v101
	v_exp_f32_e32 v103, v103
	v_pk_mul_f32 v[108:109], v[146:147], v[168:169]
	v_lshlrev_b32_e32 v113, 16, v70
	v_mov_b32_e32 v112, v83
	v_add_f32_e32 v103, 1.0, v103
	v_rcp_f32_e32 v103, v103
	s_nop 0
	v_mul_f32_e32 v101, v101, v103
	v_mul_f32_e32 v103, 0x3d800000, v101
	v_cndmask_b32_e64 v101, v101, v103, s[18:19]
	v_add_f32_e32 v103, v110, v111
	v_add_f32_e32 v103, v103, v108
	v_add_f32_e32 v103, v103, v109
	v_mul_f32_e32 v108, 0xbfb8aa3b, v103
	v_exp_f32_e32 v108, v108
	s_nop 0
	v_add_f32_e32 v108, 1.0, v108
	v_rcp_f32_e32 v108, v108
	s_nop 0
	v_mul_f32_e32 v103, v103, v108
	v_mul_f32_e32 v108, 0x3d800000, v103
	v_cndmask_b32_e64 v103, v103, v108, s[18:19]
	v_pk_mul_f32 v[108:109], v[150:151], v[92:93]
	v_pk_mov_b32 v[92:93], v[92:93], v[170:171] op_sel:[1,0]
	s_nop 0
	v_pk_mul_f32 v[110:111], v[54:55], v[92:93]
	s_nop 0
	v_add_f32_e32 v76, v76, v110
	v_add_f32_e32 v76, v76, v111
	v_mul_f32_e32 v80, 0xbfb8aa3b, v76
	v_exp_f32_e32 v80, v80
	v_and_b32_e32 v111, 0xffff0000, v70
	v_mov_b32_e32 v110, v117
	v_add_f32_e32 v80, 1.0, v80
	v_rcp_f32_e32 v80, v80
	s_nop 0
	v_mul_f32_e32 v76, v76, v80
	v_mul_f32_e32 v80, 0x3d800000, v76
	v_cndmask_b32_e64 v76, v76, v80, s[18:19]
	v_add_f32_e32 v80, v108, v109
	v_add_f32_e32 v80, v80, v106
	v_add_f32_e32 v80, v80, v107
	v_cvt_pk_bf16_f32 v76, v101, v76
	v_mul_f32_e32 v101, 0xbfb8aa3b, v80
	v_exp_f32_e32 v101, v101
	v_pk_mul_f32 v[106:107], v[142:143], v[90:91]
	v_pk_mov_b32 v[90:91], v[90:91], v[172:173] op_sel:[1,0]
	v_add_f32_e32 v101, 1.0, v101
	v_rcp_f32_e32 v101, v101
	v_pk_mul_f32 v[108:109], v[140:141], v[90:91]
	v_mul_f32_e32 v80, v80, v101
	v_mul_f32_e32 v101, 0x3d800000, v80
	v_cndmask_b32_e64 v101, v80, v101, s[18:19]
	v_add_f32_e32 v80, v104, v105
	v_add_f32_e32 v80, v80, v108
	v_add_f32_e32 v80, v80, v109
	v_mul_f32_e32 v104, 0xbfb8aa3b, v80
	v_exp_f32_e32 v104, v104
	v_lshlrev_b32_e32 v109, 16, v71
	v_add_f32_e32 v104, 1.0, v104
	v_rcp_f32_e32 v104, v104
	s_nop 0
	v_mul_f32_e32 v80, v80, v104
	v_mul_f32_e32 v104, 0x3d800000, v80
	v_cndmask_b32_e64 v108, v80, v104, s[18:19]
	v_pk_mul_f32 v[104:105], v[140:141], v[172:173]
	v_add_f32_e32 v80, v106, v107
	v_add_f32_e32 v80, v80, v104
	v_add_f32_e32 v80, v80, v105
	v_mul_f32_e32 v104, 0xbfb8aa3b, v80
	v_exp_f32_e32 v104, v104
	v_and_b32_e32 v107, 0xffff0000, v71
	v_pk_mul_f32 v[70:71], v[160:161], v[114:115]
	v_add_f32_e32 v104, 1.0, v104
	v_rcp_f32_e32 v104, v104
	v_add_f32_e32 v70, v70, v71
	v_mul_f32_e32 v80, v80, v104
	v_mul_f32_e32 v104, 0x3d800000, v80
	v_cndmask_b32_e64 v106, v80, v104, s[18:19]
	v_pk_mov_b32 v[80:81], v[86:87], v[174:175] op_sel:[1,0]
	v_pk_mul_f32 v[104:105], v[144:145], v[86:87]
	v_pk_mul_f32 v[86:87], v[56:57], v[80:81]
	s_nop 0
	v_add_f32_e32 v77, v77, v86
	v_add_f32_e32 v77, v77, v87
	v_mul_f32_e32 v86, 0xbfb8aa3b, v77
	v_exp_f32_e32 v86, v86
	s_nop 0
	v_add_f32_e32 v86, 1.0, v86
	v_rcp_f32_e32 v86, v86
	s_nop 0
	v_mul_f32_e32 v77, v77, v86
	v_mul_f32_e32 v86, 0x3d800000, v77
	v_cndmask_b32_e64 v77, v77, v86, s[18:19]
	v_cvt_pk_bf16_f32 v77, v108, v77
	global_store_dwordx4 v[84:85], v[74:77], off
	v_or_b32_e32 v84, 0x5800, v164
	v_mov_b32_e32 v85, v165
	v_pk_mul_f32 v[74:75], v[56:57], v[174:175]
	v_add_f32_e32 v76, v104, v105
	v_add_f32_e32 v74, v76, v74
	v_add_f32_e32 v74, v74, v75
	v_mul_f32_e32 v75, 0xbfb8aa3b, v74
	v_exp_f32_e32 v75, v75
	v_lshlrev_b32_e32 v105, 16, v72
	v_lshl_add_u64 v[84:85], v[138:139], 0, v[84:85]
	v_mov_b32_e32 v108, v121
	v_add_f32_e32 v75, 1.0, v75
	v_rcp_f32_e32 v75, v75
	v_mov_b32_e32 v104, v169
	v_mul_f32_e32 v74, v74, v75
	v_mul_f32_e32 v75, 0x3d800000, v74
	v_cndmask_b32_e64 v77, v74, v75, s[18:19]
	v_cvt_pk_bf16_f32 v74, v102, v100
	v_cvt_pk_bf16_f32 v75, v98, v99
	v_cvt_pk_bf16_f32 v76, v103, v101
	v_and_b32_e32 v103, 0xffff0000, v72
	v_lshlrev_b32_e32 v101, 16, v73
	v_and_b32_e32 v99, 0xffff0000, v73
	v_pk_mul_f32 v[72:73], v[158:159], v[112:113]
	v_cvt_pk_bf16_f32 v77, v106, v77
	global_store_dwordx4 v[84:85], v[74:77], off
	v_add_f32_e32 v70, v70, v72
	v_add_f32_e32 v70, v70, v73
	v_mul_f32_e32 v71, 0xbfb8aa3b, v70
	v_exp_f32_e32 v71, v71
	v_pk_mul_f32 v[72:73], v[50:51], v[110:111]
	v_mov_b32_e32 v106, v79
	v_mov_b32_e32 v102, v171
	v_add_f32_e32 v71, 1.0, v71
	v_rcp_f32_e32 v71, v71
	v_mov_b32_e32 v100, v173
	v_mov_b32_e32 v98, v175
	v_mul_f32_e32 v70, v70, v71
	v_mul_f32_e32 v71, 0x3d800000, v70
	v_cndmask_b32_e64 v74, v70, v71, s[18:19]
	v_pk_mul_f32 v[70:71], v[162:163], v[118:119]
	s_nop 0
	v_add_f32_e32 v70, v70, v71
	v_add_f32_e32 v70, v70, v72
	v_add_f32_e32 v70, v70, v73
	v_mul_f32_e32 v71, 0xbfb8aa3b, v70
	v_exp_f32_e32 v71, v71
	v_pk_mul_f32 v[72:73], v[152:153], v[108:109]
	v_add_f32_e32 v71, 1.0, v71
	v_rcp_f32_e32 v71, v71
	s_nop 0
	v_mul_f32_e32 v70, v70, v71
	v_mul_f32_e32 v71, 0x3d800000, v70
	v_cndmask_b32_e64 v75, v70, v71, s[18:19]
	v_pk_mul_f32 v[70:71], v[154:155], v[166:167]
	v_and_b32_e32 v167, 0xffff0000, v69
	v_add_f32_e32 v70, v70, v71
	v_add_f32_e32 v70, v70, v72
	v_add_f32_e32 v70, v70, v73
	v_mul_f32_e32 v71, 0xbfb8aa3b, v70
	v_exp_f32_e32 v71, v71
	v_pk_mul_f32 v[72:73], v[52:53], v[106:107]
	v_and_b32_e32 v166, 0xffff0000, v65
	v_add_f32_e32 v71, 1.0, v71
	v_rcp_f32_e32 v71, v71
	s_nop 0
	v_mul_f32_e32 v70, v70, v71
	v_mul_f32_e32 v71, 0x3d800000, v70
	v_cndmask_b32_e64 v76, v70, v71, s[18:19]
	v_pk_mul_f32 v[70:71], v[156:157], v[96:97]
	v_pk_mul_f32 v[96:97], v[142:143], v[172:173]
	v_add_f32_e32 v70, v70, v71
	v_add_f32_e32 v70, v70, v72
	v_add_f32_e32 v70, v70, v73
	v_mul_f32_e32 v71, 0xbfb8aa3b, v70
	v_exp_f32_e32 v71, v71
	v_pk_mul_f32 v[72:73], v[146:147], v[104:105]
	v_lshlrev_b32_e32 v173, 16, v68
	v_lshlrev_b32_e32 v172, 16, v64
	v_add_f32_e32 v71, 1.0, v71
	v_rcp_f32_e32 v71, v71
	s_nop 0
	v_mul_f32_e32 v70, v70, v71
	v_mul_f32_e32 v71, 0x3d800000, v70
	v_cndmask_b32_e64 v77, v70, v71, s[18:19]
	v_pk_mul_f32 v[70:71], v[148:149], v[94:95]
	s_nop 0
	v_add_f32_e32 v70, v70, v71
	v_add_f32_e32 v70, v70, v72
	v_add_f32_e32 v70, v70, v73
	v_mul_f32_e32 v71, 0xbfb8aa3b, v70
	v_exp_f32_e32 v71, v71
	v_pk_mul_f32 v[72:73], v[54:55], v[102:103]
	v_add_f32_e32 v71, 1.0, v71
	v_rcp_f32_e32 v71, v71
	s_nop 0
	v_mul_f32_e32 v70, v70, v71
	v_mul_f32_e32 v71, 0x3d800000, v70
	v_cndmask_b32_e64 v84, v70, v71, s[18:19]
	v_pk_mul_f32 v[70:71], v[150:151], v[92:93]
	s_nop 0
	v_add_f32_e32 v70, v70, v71
	v_add_f32_e32 v70, v70, v72
	v_add_f32_e32 v70, v70, v73
	v_mul_f32_e32 v71, 0xbfb8aa3b, v70
	v_exp_f32_e32 v71, v71
	v_pk_mul_f32 v[72:73], v[140:141], v[100:101]
	v_add_f32_e32 v71, 1.0, v71
	v_rcp_f32_e32 v71, v71
	s_nop 0
	v_mul_f32_e32 v70, v70, v71
	v_mul_f32_e32 v71, 0x3d800000, v70
	v_cndmask_b32_e64 v85, v70, v71, s[18:19]
	v_pk_mul_f32 v[70:71], v[142:143], v[90:91]
	s_nop 0
	v_add_f32_e32 v70, v70, v71
	v_add_f32_e32 v70, v70, v72
	v_add_f32_e32 v70, v70, v73
	v_mul_f32_e32 v71, 0xbfb8aa3b, v70
	v_exp_f32_e32 v71, v71
	v_pk_mul_f32 v[72:73], v[56:57], v[98:99]
	v_add_f32_e32 v71, 1.0, v71
	v_rcp_f32_e32 v71, v71
	s_nop 0
	v_mul_f32_e32 v70, v70, v71
	v_mul_f32_e32 v71, 0x3d800000, v70
	v_cndmask_b32_e64 v86, v70, v71, s[18:19]
	v_pk_mul_f32 v[70:71], v[144:145], v[80:81]
	v_pk_mul_f32 v[80:81], v[150:151], v[170:171]
	v_add_f32_e32 v70, v70, v71
	v_add_f32_e32 v70, v70, v72
	v_add_f32_e32 v70, v70, v73
	v_mul_f32_e32 v71, 0xbfb8aa3b, v70
	v_exp_f32_e32 v71, v71
	v_and_b32_e32 v171, 0xffff0000, v68
	v_and_b32_e32 v170, 0xffff0000, v64
	v_add_f32_e32 v64, v80, v81
	v_add_f32_e32 v71, 1.0, v71
	v_rcp_f32_e32 v71, v71
	s_nop 0
	v_mul_f32_e32 v70, v70, v71
	v_mul_f32_e32 v71, 0x3d800000, v70
	v_cndmask_b32_e64 v73, v70, v71, s[18:19]
	v_cvt_pk_bf16_f32 v70, v74, v75
	v_or_b32_e32 v74, 0x6000, v164
	v_mov_b32_e32 v75, v165
	v_cvt_pk_bf16_f32 v71, v76, v77
	v_lshl_add_u64 v[74:75], v[138:139], 0, v[74:75]
	v_cvt_pk_bf16_f32 v72, v84, v85
	v_cvt_pk_bf16_f32 v73, v86, v73
	global_store_dwordx4 v[74:75], v[70:73], off
	v_pk_mul_f32 v[74:75], v[162:163], v[116:117]
	v_pk_mul_f32 v[116:117], v[144:145], v[174:175]
	v_or_b32_e32 v70, 0x6800, v164
	v_mov_b32_e32 v71, v165
	v_lshl_add_u64 v[114:115], v[138:139], 0, v[70:71]
	v_pk_mov_b32 v[70:71], v[180:181], v[180:181] op_sel:[1,0]
	v_pk_mul_f32 v[72:73], v[160:161], v[82:83]
	v_mov_b32_e32 v82, v113
	v_mov_b32_e32 v83, v71
	v_pk_mul_f32 v[84:85], v[158:159], v[82:83]
	v_add_f32_e32 v71, v72, v73
	v_add_f32_e32 v71, v71, v84
	v_add_f32_e32 v71, v71, v85
	v_mul_f32_e32 v72, 0xbfb8aa3b, v71
	v_exp_f32_e32 v72, v72
	v_mov_b32_e32 v84, v111
	v_add_f32_e32 v62, v74, v75
	v_pk_mov_b32 v[74:75], v[176:177], v[176:177] op_sel:[1,0]
	v_add_f32_e32 v72, 1.0, v72
	v_rcp_f32_e32 v72, v72
	v_and_b32_e32 v175, 0xffff0000, v67
	v_and_b32_e32 v174, 0xffff0000, v63
	v_pk_mul_f32 v[76:77], v[156:157], v[78:79]
	v_mul_f32_e32 v71, v71, v72
	v_mul_f32_e32 v72, 0x3d800000, v71
	v_cndmask_b32_e64 v71, v71, v72, s[18:19]
	v_pk_mov_b32 v[72:73], v[178:179], v[178:179] op_sel:[1,0]
	v_add_f32_e32 v63, v76, v77
	v_mov_b32_e32 v85, v73
	v_pk_mul_f32 v[86:87], v[50:51], v[84:85]
	v_pk_mov_b32 v[76:77], v[172:173], v[172:173] op_sel:[1,0]
	v_add_f32_e32 v62, v62, v86
	v_add_f32_e32 v62, v62, v87
	v_mul_f32_e32 v66, 0xbfb8aa3b, v62
	v_exp_f32_e32 v66, v66
	v_mov_b32_e32 v86, v109
	v_mov_b32_e32 v87, v75
	v_pk_mul_f32 v[90:91], v[152:153], v[86:87]
	v_add_f32_e32 v66, 1.0, v66
	v_rcp_f32_e32 v66, v66
	v_pk_mul_f32 v[78:79], v[148:149], v[168:169]
	v_lshlrev_b32_e32 v169, 16, v69
	v_lshlrev_b32_e32 v168, 16, v65
	v_mul_f32_e32 v62, v62, v66
	v_mul_f32_e32 v66, 0x3d800000, v62
	v_cndmask_b32_e64 v62, v62, v66, s[18:19]
	v_add_f32_e32 v66, v88, v89
	v_add_f32_e32 v66, v66, v90
	v_add_f32_e32 v66, v66, v91
	v_cvt_pk_bf16_f32 v62, v71, v62
	v_mul_f32_e32 v71, 0xbfb8aa3b, v66
	v_exp_f32_e32 v71, v71
	v_mov_b32_e32 v88, v107
	v_pk_mov_b32 v[80:81], v[168:169], v[168:169] op_sel:[1,0]
	v_add_f32_e32 v65, v116, v117
	v_add_f32_e32 v71, 1.0, v71
	v_rcp_f32_e32 v71, v71
	s_nop 0
	v_mul_f32_e32 v66, v66, v71
	v_mul_f32_e32 v71, 0x3d800000, v66
	v_cndmask_b32_e64 v71, v66, v71, s[18:19]
	v_pk_mov_b32 v[66:67], v[174:175], v[174:175] op_sel:[1,0]
	s_nop 0
	v_mov_b32_e32 v89, v67
	v_pk_mul_f32 v[90:91], v[52:53], v[88:89]
	s_nop 0
	v_add_f32_e32 v63, v63, v90
	v_add_f32_e32 v63, v63, v91
	v_mul_f32_e32 v67, 0xbfb8aa3b, v63
	v_exp_f32_e32 v67, v67
	v_mov_b32_e32 v90, v105
	v_mov_b32_e32 v91, v77
	v_pk_mul_f32 v[92:93], v[146:147], v[90:91]
	v_add_f32_e32 v67, 1.0, v67
	v_rcp_f32_e32 v67, v67
	s_nop 0
	v_mul_f32_e32 v63, v63, v67
	v_mul_f32_e32 v67, 0x3d800000, v63
	v_cndmask_b32_e64 v63, v63, v67, s[18:19]
	v_add_f32_e32 v67, v78, v79
	v_add_f32_e32 v67, v67, v92
	v_pk_mov_b32 v[78:79], v[170:171], v[170:171] op_sel:[1,0]
	v_add_f32_e32 v67, v67, v93
	v_mov_b32_e32 v92, v103
	v_mov_b32_e32 v93, v79
	v_pk_mul_f32 v[94:95], v[54:55], v[92:93]
	v_cvt_pk_bf16_f32 v63, v71, v63
	v_mul_f32_e32 v71, 0xbfb8aa3b, v67
	v_add_f32_e32 v64, v64, v94
	v_add_f32_e32 v64, v64, v95
	v_mul_f32_e32 v68, 0xbfb8aa3b, v64
	v_exp_f32_e32 v71, v71
	v_exp_f32_e32 v68, v68
	v_mov_b32_e32 v94, v101
	v_mov_b32_e32 v95, v81
	v_add_f32_e32 v71, 1.0, v71
	v_add_f32_e32 v68, 1.0, v68
	v_rcp_f32_e32 v71, v71
	v_rcp_f32_e32 v68, v68
	v_pk_mul_f32 v[118:119], v[140:141], v[94:95]
	s_waitcnt vmcnt(13)
	v_lshlrev_b32_e32 v81, 16, v61
	v_mul_f32_e32 v67, v67, v71
	v_mul_f32_e32 v64, v64, v68
	v_mul_f32_e32 v71, 0x3d800000, v67
	v_mul_f32_e32 v68, 0x3d800000, v64
	v_cndmask_b32_e64 v67, v67, v71, s[18:19]
	v_cndmask_b32_e64 v64, v64, v68, s[18:19]
	v_cvt_pk_bf16_f32 v64, v67, v64
	v_add_f32_e32 v67, v96, v97
	v_add_f32_e32 v67, v67, v118
	v_add_f32_e32 v67, v67, v119
	v_mul_f32_e32 v68, 0xbfb8aa3b, v67
	v_exp_f32_e32 v68, v68
	v_mov_b32_e32 v96, v99
	v_mov_b32_e32 v194, v81
	v_add_f32_e32 v68, 1.0, v68
	v_rcp_f32_e32 v68, v68
	s_nop 0
	v_mul_f32_e32 v67, v67, v68
	v_mul_f32_e32 v68, 0x3d800000, v67
	v_cndmask_b32_e64 v67, v67, v68, s[18:19]
	v_pk_mov_b32 v[68:69], v[166:167], v[166:167] op_sel:[1,0]
	s_nop 0
	v_mov_b32_e32 v97, v69
	v_pk_mul_f32 v[118:119], v[56:57], v[96:97]
	s_nop 0
	v_add_f32_e32 v65, v65, v118
	v_add_f32_e32 v65, v65, v119
	v_mul_f32_e32 v69, 0xbfb8aa3b, v65
	v_exp_f32_e32 v69, v69
	s_nop 0
	v_add_f32_e32 v69, 1.0, v69
	v_rcp_f32_e32 v69, v69
	s_nop 0
	v_mul_f32_e32 v65, v65, v69
	v_mul_f32_e32 v69, 0x3d800000, v65
	v_cndmask_b32_e64 v65, v65, v69, s[18:19]
	v_cvt_pk_bf16_f32 v65, v67, v65
	global_store_dwordx4 v[114:115], v[62:65], off
	s_nop 1
	v_pk_mul_f32 v[62:63], v[160:161], v[112:113]
	v_pk_mul_f32 v[64:65], v[158:159], v[180:181]
	v_add_f32_e32 v62, v62, v63
	v_add_f32_e32 v62, v62, v64
	v_add_f32_e32 v62, v62, v65
	v_mul_f32_e32 v63, 0xbfb8aa3b, v62
	v_exp_f32_e32 v63, v63
	v_pk_mul_f32 v[64:65], v[50:51], v[178:179]
	v_add_f32_e32 v63, 1.0, v63
	v_rcp_f32_e32 v63, v63
	s_nop 0
	v_mul_f32_e32 v62, v62, v63
	v_mul_f32_e32 v63, 0x3d800000, v62
	v_cndmask_b32_e64 v67, v62, v63, s[18:19]
	v_pk_mul_f32 v[62:63], v[162:163], v[110:111]
	s_nop 0
	v_add_f32_e32 v62, v62, v63
	v_add_f32_e32 v62, v62, v64
	v_add_f32_e32 v62, v62, v65
	v_mul_f32_e32 v63, 0xbfb8aa3b, v62
	v_exp_f32_e32 v63, v63
	v_pk_mul_f32 v[64:65], v[152:153], v[176:177]
	v_add_f32_e32 v63, 1.0, v63
	v_rcp_f32_e32 v63, v63
	s_nop 0
	v_mul_f32_e32 v62, v62, v63
	v_mul_f32_e32 v63, 0x3d800000, v62
	v_cndmask_b32_e64 v69, v62, v63, s[18:19]
	v_pk_mul_f32 v[62:63], v[154:155], v[108:109]
	s_nop 0
	v_add_f32_e32 v62, v62, v63
	v_add_f32_e32 v62, v62, v64
	v_add_f32_e32 v62, v62, v65
	v_mul_f32_e32 v63, 0xbfb8aa3b, v62
	v_exp_f32_e32 v63, v63
	v_pk_mul_f32 v[64:65], v[52:53], v[174:175]
	v_add_f32_e32 v63, 1.0, v63
	v_rcp_f32_e32 v63, v63
	s_nop 0
	v_mul_f32_e32 v62, v62, v63
	v_mul_f32_e32 v63, 0x3d800000, v62
	v_cndmask_b32_e64 v71, v62, v63, s[18:19]
	v_pk_mul_f32 v[62:63], v[156:157], v[106:107]
	s_nop 0
	v_add_f32_e32 v62, v62, v63
	v_add_f32_e32 v62, v62, v64
	v_add_f32_e32 v62, v62, v65
	v_mul_f32_e32 v63, 0xbfb8aa3b, v62
	v_exp_f32_e32 v63, v63
	v_pk_mul_f32 v[64:65], v[146:147], v[172:173]
	v_add_f32_e32 v63, 1.0, v63
	v_rcp_f32_e32 v63, v63
	s_nop 0
	v_mul_f32_e32 v62, v62, v63
	v_mul_f32_e32 v63, 0x3d800000, v62
	v_cndmask_b32_e64 v73, v62, v63, s[18:19]
	v_pk_mul_f32 v[62:63], v[148:149], v[104:105]
	s_nop 0
	v_add_f32_e32 v62, v62, v63
	v_add_f32_e32 v62, v62, v64
	v_add_f32_e32 v62, v62, v65
	v_mul_f32_e32 v63, 0xbfb8aa3b, v62
	v_exp_f32_e32 v63, v63
	v_pk_mul_f32 v[64:65], v[54:55], v[170:171]
	v_add_f32_e32 v63, 1.0, v63
	v_rcp_f32_e32 v63, v63
	s_nop 0
	v_mul_f32_e32 v62, v62, v63
	v_mul_f32_e32 v63, 0x3d800000, v62
	v_cndmask_b32_e64 v75, v62, v63, s[18:19]
	v_pk_mul_f32 v[62:63], v[150:151], v[102:103]
	s_nop 0
	v_add_f32_e32 v62, v62, v63
	v_add_f32_e32 v62, v62, v64
	v_add_f32_e32 v62, v62, v65
	v_mul_f32_e32 v63, 0xbfb8aa3b, v62
	v_exp_f32_e32 v63, v63
	v_pk_mul_f32 v[64:65], v[140:141], v[168:169]
	v_add_f32_e32 v63, 1.0, v63
	v_rcp_f32_e32 v63, v63
	s_nop 0
	v_mul_f32_e32 v62, v62, v63
	v_mul_f32_e32 v63, 0x3d800000, v62
	v_cndmask_b32_e64 v77, v62, v63, s[18:19]
	v_pk_mul_f32 v[62:63], v[142:143], v[100:101]
	s_nop 0
	v_add_f32_e32 v62, v62, v63
	v_add_f32_e32 v62, v62, v64
	v_add_f32_e32 v62, v62, v65
	v_mul_f32_e32 v63, 0xbfb8aa3b, v62
	v_exp_f32_e32 v63, v63
	v_pk_mul_f32 v[64:65], v[56:57], v[166:167]
	v_add_f32_e32 v63, 1.0, v63
	v_rcp_f32_e32 v63, v63
	s_nop 0
	v_mul_f32_e32 v62, v62, v63
	v_mul_f32_e32 v63, 0x3d800000, v62
	v_cndmask_b32_e64 v79, v62, v63, s[18:19]
	v_pk_mul_f32 v[62:63], v[144:145], v[98:99]
	v_or_b32_e32 v98, 0x7000, v164
	v_add_f32_e32 v62, v62, v63
	v_add_f32_e32 v62, v62, v64
	v_add_f32_e32 v62, v62, v65
	v_mul_f32_e32 v63, 0xbfb8aa3b, v62
	v_exp_f32_e32 v63, v63
	v_mov_b32_e32 v99, v165
	v_lshl_add_u64 v[98:99], v[138:139], 0, v[98:99]
	v_or_b32_e32 v164, 0x7800, v164
	v_add_f32_e32 v63, 1.0, v63
	v_rcp_f32_e32 v63, v63
	s_nop 0
	v_mul_f32_e32 v62, v62, v63
	v_mul_f32_e32 v63, 0x3d800000, v62
	v_cndmask_b32_e64 v65, v62, v63, s[18:19]
	v_cvt_pk_bf16_f32 v62, v67, v69
	v_cvt_pk_bf16_f32 v63, v71, v73
	v_cvt_pk_bf16_f32 v64, v75, v77
	v_lshlrev_b32_e32 v71, 16, v58
	v_and_b32_e32 v73, 0xffff0000, v58
	v_lshlrev_b32_e32 v75, 16, v59
	v_and_b32_e32 v67, 0xffff0000, v59
	v_pk_mul_f32 v[58:59], v[160:161], v[82:83]
	v_cvt_pk_bf16_f32 v65, v79, v65
	v_lshlrev_b32_e32 v77, 16, v60
	v_and_b32_e32 v79, 0xffff0000, v60
	v_and_b32_e32 v69, 0xffff0000, v61
	v_pk_mul_f32 v[60:61], v[158:159], v[70:71]
	v_add_f32_e32 v58, v58, v59
	v_add_f32_e32 v58, v58, v60
	v_add_f32_e32 v58, v58, v61
	v_mul_f32_e32 v59, 0xbfb8aa3b, v58
	v_exp_f32_e32 v59, v59
	global_store_dwordx4 v[98:99], v[62:65], off
	v_pk_mul_f32 v[60:61], v[50:51], v[72:73]
	v_mov_b32_e32 v182, v71
	v_add_f32_e32 v59, 1.0, v59
	v_rcp_f32_e32 v59, v59
	v_mov_b32_e32 v184, v73
	v_mov_b32_e32 v186, v75
	v_mov_b32_e32 v188, v67
	v_mul_f32_e32 v58, v58, v59
	v_mul_f32_e32 v59, 0x3d800000, v58
	v_cndmask_b32_e64 v62, v58, v59, s[18:19]
	v_pk_mul_f32 v[58:59], v[162:163], v[84:85]
	v_mov_b32_e32 v190, v77
	v_add_f32_e32 v58, v58, v59
	v_add_f32_e32 v58, v58, v60
	v_add_f32_e32 v58, v58, v61
	v_mul_f32_e32 v59, 0xbfb8aa3b, v58
	v_exp_f32_e32 v59, v59
	v_pk_mul_f32 v[60:61], v[152:153], v[74:75]
	v_mov_b32_e32 v192, v79
	v_mov_b32_e32 v196, v69
	v_add_f32_e32 v59, 1.0, v59
	v_rcp_f32_e32 v59, v59
	s_nop 0
	v_mul_f32_e32 v58, v58, v59
	v_mul_f32_e32 v59, 0x3d800000, v58
	v_cndmask_b32_e64 v63, v58, v59, s[18:19]
	v_pk_mul_f32 v[58:59], v[154:155], v[86:87]
	s_nop 0
	v_add_f32_e32 v58, v58, v59
	v_add_f32_e32 v58, v58, v60
	v_add_f32_e32 v58, v58, v61
	v_mul_f32_e32 v59, 0xbfb8aa3b, v58
	v_exp_f32_e32 v59, v59
	v_pk_mul_f32 v[60:61], v[52:53], v[66:67]
	v_add_f32_e32 v59, 1.0, v59
	v_rcp_f32_e32 v59, v59
	s_nop 0
	v_mul_f32_e32 v58, v58, v59
	v_mul_f32_e32 v59, 0x3d800000, v58
	v_cndmask_b32_e64 v64, v58, v59, s[18:19]
	v_pk_mul_f32 v[58:59], v[156:157], v[88:89]
	s_nop 0
	v_add_f32_e32 v58, v58, v59
	v_add_f32_e32 v58, v58, v60
	v_add_f32_e32 v58, v58, v61
	v_mul_f32_e32 v59, 0xbfb8aa3b, v58
	v_exp_f32_e32 v59, v59
	v_pk_mul_f32 v[60:61], v[146:147], v[76:77]
	v_add_f32_e32 v59, 1.0, v59
	v_rcp_f32_e32 v59, v59
	s_nop 0
	v_mul_f32_e32 v58, v58, v59
	v_mul_f32_e32 v59, 0x3d800000, v58
	v_cndmask_b32_e64 v65, v58, v59, s[18:19]
	v_pk_mul_f32 v[58:59], v[148:149], v[90:91]
	s_nop 0
	v_add_f32_e32 v58, v58, v59
	v_add_f32_e32 v58, v58, v60
	v_add_f32_e32 v58, v58, v61
	v_mul_f32_e32 v59, 0xbfb8aa3b, v58
	v_exp_f32_e32 v59, v59
	v_pk_mul_f32 v[60:61], v[54:55], v[78:79]
	v_add_f32_e32 v59, 1.0, v59
	v_rcp_f32_e32 v59, v59
	s_nop 0
	v_mul_f32_e32 v58, v58, v59
	v_mul_f32_e32 v59, 0x3d800000, v58
	v_cndmask_b32_e64 v66, v58, v59, s[18:19]
	v_pk_mul_f32 v[58:59], v[150:151], v[92:93]
	s_nop 0
	v_add_f32_e32 v58, v58, v59
	v_add_f32_e32 v58, v58, v60
	v_add_f32_e32 v58, v58, v61
	v_mul_f32_e32 v59, 0xbfb8aa3b, v58
	v_exp_f32_e32 v59, v59
	v_pk_mul_f32 v[60:61], v[140:141], v[80:81]
	v_add_f32_e32 v59, 1.0, v59
	v_rcp_f32_e32 v59, v59
	s_nop 0
	v_mul_f32_e32 v58, v58, v59
	v_mul_f32_e32 v59, 0x3d800000, v58
	v_cndmask_b32_e64 v70, v58, v59, s[18:19]
	v_pk_mul_f32 v[58:59], v[142:143], v[94:95]
	s_nop 0
	v_add_f32_e32 v58, v58, v59
	v_add_f32_e32 v58, v58, v60
	v_add_f32_e32 v58, v58, v61
	v_mul_f32_e32 v59, 0xbfb8aa3b, v58
	v_exp_f32_e32 v59, v59
	v_pk_mul_f32 v[60:61], v[56:57], v[68:69]
	v_add_f32_e32 v59, 1.0, v59
	v_rcp_f32_e32 v59, v59
	s_nop 0
	v_mul_f32_e32 v58, v58, v59
	v_mul_f32_e32 v59, 0x3d800000, v58
	v_cndmask_b32_e64 v72, v58, v59, s[18:19]
	v_pk_mul_f32 v[58:59], v[144:145], v[96:97]
	s_nop 0
	v_add_f32_e32 v58, v58, v59
	v_add_f32_e32 v58, v58, v60
	v_add_f32_e32 v58, v58, v61
	v_mul_f32_e32 v59, 0xbfb8aa3b, v58
	v_exp_f32_e32 v59, v59
	s_nop 0
	v_add_f32_e32 v59, 1.0, v59
	v_rcp_f32_e32 v59, v59
	s_nop 0
	v_mul_f32_e32 v58, v58, v59
	v_mul_f32_e32 v59, 0x3d800000, v58
	v_cndmask_b32_e64 v61, v58, v59, s[18:19]
	v_cvt_pk_bf16_f32 v58, v62, v63
	v_lshl_add_u64 v[62:63], v[138:139], 0, v[164:165]
	v_cvt_pk_bf16_f32 v59, v64, v65
	v_cvt_pk_bf16_f32 v60, v66, v70
	v_cvt_pk_bf16_f32 v61, v72, v61
	global_store_dwordx4 v[62:63], v[58:61], off
	s_cbranch_vccz .LBB0_445
	s_and_saveexec_b64 s[18:19], s[4:5]
	s_cbranch_execz .LBB0_448
	v_mov_b32_e32 v6, v0
	v_mov_b64_e32 v[4:5], s[60:61]
	v_and_b32_e32 v2, 7, v6
	v_lshlrev_b32_e32 v2, 3, v2
	v_ashrrev_i32_e32 v3, 31, v2
	v_lshl_add_u64 v[2:3], s[42:43], 0, v[2:3]
	v_mad_u64_u32 v[4:5], s[20:21], v2, s93, v[4:5]
	v_lshlrev_b32_e32 v2, 1, v6
	v_mad_i32_i24 v5, v3, s93, v5
	v_and_b32_e32 v126, 0x1f0, v2
	v_lshl_add_u64 v[26:27], v[4:5], 0, v[126:127]
	v_add_co_u32_e32 v2, vcc, s96, v26
	s_movk_i32 s20, 0x7000
	s_nop 0
	v_addc_co_u32_e32 v3, vcc, 0, v27, vcc
	v_add_co_u32_e32 v6, vcc, s20, v26
	s_mov_b32 s20, 0xc000
	s_nop 0
	v_addc_co_u32_e32 v7, vcc, 0, v27, vcc
	v_add_co_u32_e32 v10, vcc, s20, v26
	s_mov_b32 s20, 0x10000
	s_nop 0
	v_addc_co_u32_e32 v11, vcc, 0, v27, vcc
	v_add_co_u32_e32 v14, vcc, s20, v26
	s_mov_b32 s20, 0x15000
	s_nop 0
	v_addc_co_u32_e32 v15, vcc, 0, v27, vcc
	v_add_co_u32_e32 v18, vcc, s20, v26
	s_mov_b32 s20, 0x1a000
	s_nop 0
	v_addc_co_u32_e32 v19, vcc, 0, v27, vcc
	v_add_co_u32_e32 v22, vcc, s20, v26
	global_load_dwordx4 v[2:5], v[2:3], off offset:2560
	s_nop 0
	global_load_dwordx4 v[6:9], v[6:7], off offset:1536
	v_addc_co_u32_e32 v23, vcc, 0, v27, vcc
	v_add_co_u32_e32 v28, vcc, 0x1f000, v26
	global_load_dwordx4 v[10:13], v[10:11], off offset:512
	s_nop 0
	global_load_dwordx4 v[14:17], v[14:15], off offset:3584
	v_addc_co_u32_e32 v29, vcc, 0, v27, vcc
	v_add_co_u32_e32 v30, vcc, 0x23000, v26
	global_load_dwordx4 v[18:21], v[18:19], off offset:2560
	s_nop 0
	global_load_dwordx4 v[22:25], v[22:23], off offset:1536
	v_addc_co_u32_e32 v31, vcc, 0, v27, vcc
	global_load_dwordx4 v[26:29], v[28:29], off offset:512
	s_nop 0
	global_load_dwordx4 v[30:33], v[30:31], off offset:3584

.LBB0_449:
	global_load_dwordx4 v[184:187], v[86:87], off
	global_load_dwordx4 v[188:191], v[82:83], off
	v_add_u32_e32 v164, s90, v46
	v_cvt_f32_u32_e32 v126, v164
	v_add_u32_e32 v164, 1, v164
	v_cvt_f32_u32_e32 v164, v164
	v_lshl_add_u64 v[192:193], v[84:85], 0, s[90:91]
	v_mul_f32_e32 v153, v47, v126
	v_mul_f32_e32 v153, 0.15915494, v153
	v_mul_f32_e32 v165, v47, v164
	v_mul_f32_e32 v165, 0.15915494, v165
	v_sin_f32_e32 v171, v153
	v_sin_f32_e32 v183, v165
	v_cos_f32_e32 v170, v153
	v_cos_f32_e32 v182, v165
	v_mul_f32_e32 v153, v49, v126
	v_mul_f32_e32 v165, v49, v164
	v_mul_f32_e32 v153, 0.15915494, v153
	v_mul_f32_e32 v165, 0.15915494, v165
	v_sin_f32_e32 v167, v153
	v_sin_f32_e32 v181, v165
	v_cos_f32_e32 v166, v153
	v_cos_f32_e32 v180, v165
	v_mul_f32_e32 v153, v53, v126
	v_mul_f32_e32 v165, v53, v164
	v_mul_f32_e32 v153, 0.15915494, v153
	v_mul_f32_e32 v165, 0.15915494, v165
	v_sin_f32_e32 v163, v153
	v_sin_f32_e32 v179, v165
	v_cos_f32_e32 v162, v153
	v_cos_f32_e32 v178, v165
	v_mul_f32_e32 v153, v57, v126
	v_mul_f32_e32 v165, v57, v164
	v_mul_f32_e32 v153, 0.15915494, v153
	v_mul_f32_e32 v165, 0.15915494, v165
	v_sin_f32_e32 v161, v153
	v_sin_f32_e32 v177, v165
	v_cos_f32_e32 v160, v153
	v_cos_f32_e32 v176, v165
	v_mul_f32_e32 v153, v61, v126
	v_mul_f32_e32 v165, v61, v164
	v_mul_f32_e32 v153, 0.15915494, v153
	v_mul_f32_e32 v165, 0.15915494, v165
	v_sin_f32_e32 v159, v153
	v_sin_f32_e32 v175, v165
	v_cos_f32_e32 v158, v153
	v_cos_f32_e32 v174, v165
	v_mul_f32_e32 v153, v65, v126
	v_mul_f32_e32 v165, v65, v164
	v_mul_f32_e32 v153, 0.15915494, v153
	v_mul_f32_e32 v165, 0.15915494, v165
	v_sin_f32_e32 v157, v153
	v_sin_f32_e32 v173, v165
	v_cos_f32_e32 v156, v153
	v_cos_f32_e32 v172, v165
	v_mul_f32_e32 v153, v96, v126
	v_mul_f32_e32 v165, v96, v164
	v_mul_f32_e32 v153, 0.15915494, v153
	v_mul_f32_e32 v165, 0.15915494, v165
	v_sin_f32_e32 v155, v153
	v_sin_f32_e32 v169, v165
	v_mul_f32_e32 v126, v97, v126
	v_mul_f32_e32 v164, v97, v164
	v_cos_f32_e32 v154, v153
	v_mul_f32_e32 v153, 0.15915494, v126
	v_cos_f32_e32 v168, v165
	v_mul_f32_e32 v165, 0.15915494, v164
	v_cos_f32_e32 v126, v153
	v_sin_f32_e32 v153, v153
	v_cos_f32_e32 v164, v165
	v_sin_f32_e32 v165, v165
	v_lshlrev_b64 v[192:193], v48, v[192:193]
	global_load_dwordx4 v[42:45], v[78:79], off
	global_load_dwordx4 v[38:41], v[74:75], off
	global_load_dwordx4 v[34:37], v[70:71], off
	v_lshl_add_u64 v[192:193], v[50:51], 0, v[192:193]
	v_lshl_add_u64 v[94:95], v[80:81], 0, s[90:91]
	v_lshlrev_b64 v[94:95], v52, v[94:95]
	v_lshl_add_u64 v[94:95], v[54:55], 0, v[94:95]
	v_lshl_add_u64 v[92:93], v[76:77], 0, s[90:91]
	s_waitcnt vmcnt(4)
	v_lshlrev_b32_e32 v195, 16, v185
	v_lshlrev_b32_e32 v194, 16, v184
	v_and_b32_e32 v185, 0xffff0000, v185
	v_and_b32_e32 v184, 0xffff0000, v184
	v_pk_mul_f32 v[196:197], v[184:185], v[184:185]
	v_lshlrev_b32_e32 v199, 16, v187
	v_lshlrev_b32_e32 v198, 16, v186
	v_and_b32_e32 v187, 0xffff0000, v187
	v_and_b32_e32 v186, 0xffff0000, v186
	v_pk_fma_f32 v[196:197], v[194:195], v[194:195], v[196:197]
	v_pk_mul_f32 v[200:201], v[186:187], v[186:187]
	v_add_f32_e32 v196, v196, v197
	v_pk_fma_f32 v[200:201], v[198:199], v[198:199], v[200:201]
	v_lshlrev_b64 v[92:93], v56, v[92:93]
	v_add_f32_e32 v196, v200, v196
	v_add_f32_e32 v196, v201, v196
	ds_bpermute_b32 v197, v98, v196
	v_cndmask_b32_e64 v201, v171, v183, s[18:19]
	v_cndmask_b32_e64 v200, v170, v182, s[18:19]
	v_lshl_add_u64 v[92:93], v[58:59], 0, v[92:93]
	v_lshl_add_u64 v[90:91], v[72:73], 0, s[90:91]
	s_waitcnt lgkmcnt(0)
	v_add_f32_e32 v196, v196, v197
	ds_bpermute_b32 v197, v99, v196
	v_lshl_add_u64 v[88:89], v[68:69], 0, s[90:91]
	s_add_u32 s90, s90, 2
	s_addc_u32 s91, s91, 0
	v_lshl_add_u64 v[70:71], v[70:71], 0, s[86:87]
	s_waitcnt lgkmcnt(0)
	v_add_f32_e32 v196, v196, v197
	ds_bpermute_b32 v197, v100, v196
	v_lshl_add_u64 v[74:75], v[74:75], 0, s[86:87]
	v_lshl_add_u64 v[78:79], v[78:79], 0, s[86:87]
	v_lshl_add_u64 v[82:83], v[82:83], 0, s[86:87]
	v_lshl_add_u64 v[86:87], v[86:87], 0, s[86:87]
	s_waitcnt lgkmcnt(0)
	v_add_f32_e32 v196, v196, v197
	v_fmamk_f32 v196, v196, 0x3c800000, v212
	v_cmp_gt_f32_e64 s[42:43], s52, v196
	v_mul_f32_e32 v197, 0x4b800000, v196
	s_cmp_eq_u32 s90, 8
	v_cndmask_b32_e64 v196, v196, v197, s[42:43]
	v_rsq_f32_e32 v196, v196
	s_nop 0
	v_mul_f32_e32 v197, 0x45800000, v196
	v_cndmask_b32_e64 v196, v196, v197, s[42:43]
	v_mul_f32_e32 v194, v196, v194
	v_mul_f32_e32 v194, v101, v194
	ds_bpermute_b32 v197, v100, v194
	v_mul_f32_e32 v184, v196, v184
	v_mul_f32_e32 v184, v102, v184
	v_mul_f32_e32 v195, v196, v195
	v_mul_f32_e32 v195, v103, v195
	s_waitcnt lgkmcnt(0)
	v_mul_f32_e32 v197, v201, v197
	v_cndmask_b32_e64 v197, v197, -v197, vcc
	v_fmac_f32_e32 v197, v200, v194
	v_mul_f32_e32 v194, 0x3e000000, v197
	v_cndmask_b32_e64 v194, v197, v194, s[28:29]
	ds_bpermute_b32 v197, v100, v184
	v_cndmask_b32_e64 v201, v167, v181, s[18:19]
	v_cndmask_b32_e64 v200, v166, v180, s[18:19]
	v_mul_f32_e32 v185, v196, v185
	v_mul_f32_e32 v185, v104, v185
	s_waitcnt lgkmcnt(0)
	v_mul_f32_e32 v197, v201, v197
	v_cndmask_b32_e64 v197, v197, -v197, vcc
	v_fmac_f32_e32 v197, v200, v184
	v_mul_f32_e32 v184, 0x3e000000, v197
	v_cndmask_b32_e64 v184, v197, v184, s[28:29]
	ds_bpermute_b32 v197, v100, v195
	v_cndmask_b32_e64 v201, v163, v179, s[18:19]
	v_cndmask_b32_e64 v200, v162, v178, s[18:19]
	v_mul_f32_e32 v186, v196, v186
	v_mul_f32_e32 v186, v106, v186
	s_waitcnt lgkmcnt(0)
	v_mul_f32_e32 v197, v201, v197
	v_cndmask_b32_e64 v197, v197, -v197, vcc
	v_fmac_f32_e32 v197, v200, v195
	v_mul_f32_e32 v195, 0x3e000000, v197
	v_cndmask_b32_e64 v195, v197, v195, s[28:29]
	ds_bpermute_b32 v197, v100, v185
	v_cndmask_b32_e64 v201, v161, v177, s[18:19]
	v_cndmask_b32_e64 v200, v160, v176, s[18:19]
	v_mul_f32_e32 v187, v196, v187
	v_mul_f32_e32 v187, v108, v187
	s_waitcnt lgkmcnt(0)
	v_mul_f32_e32 v197, v201, v197
	v_cndmask_b32_e64 v197, v197, -v197, vcc
	v_fmac_f32_e32 v197, v200, v185
	v_mul_f32_e32 v185, 0x3e000000, v197
	v_cndmask_b32_e64 v185, v197, v185, s[28:29]
	v_mul_f32_e32 v197, v196, v198
	v_mul_f32_e32 v197, v105, v197
	ds_bpermute_b32 v198, v100, v197
	v_cndmask_b32_e64 v201, v159, v175, s[18:19]
	v_cndmask_b32_e64 v200, v158, v174, s[18:19]
	v_cvt_pk_bf16_f32 v184, v194, v184
	v_cvt_pk_bf16_f32 v185, v195, v185
	s_waitcnt lgkmcnt(0)
	v_mul_f32_e32 v198, v201, v198
	v_cndmask_b32_e64 v198, v198, -v198, vcc
	v_fmac_f32_e32 v198, v200, v197
	v_mul_f32_e32 v197, 0x3e000000, v198
	v_cndmask_b32_e64 v197, v198, v197, s[28:29]
	ds_bpermute_b32 v198, v100, v186
	v_cndmask_b32_e64 v201, v157, v173, s[18:19]
	v_cndmask_b32_e64 v200, v156, v172, s[18:19]
	s_waitcnt lgkmcnt(0)
	v_mul_f32_e32 v198, v201, v198
	v_cndmask_b32_e64 v198, v198, -v198, vcc
	v_fmac_f32_e32 v198, v200, v186
	v_mul_f32_e32 v186, 0x3e000000, v198
	v_cndmask_b32_e64 v186, v198, v186, s[28:29]
	v_mul_f32_e32 v198, v196, v199
	v_mul_f32_e32 v198, v107, v198
	ds_bpermute_b32 v199, v100, v198
	ds_bpermute_b32 v196, v100, v187
	v_cndmask_b32_e64 v201, v155, v169, s[18:19]
	v_cndmask_b32_e64 v200, v154, v168, s[18:19]
	v_cvt_pk_bf16_f32 v186, v197, v186
	s_waitcnt lgkmcnt(1)
	v_mul_f32_e32 v199, v201, v199
	v_cndmask_b32_e64 v199, v199, -v199, vcc
	v_fmac_f32_e32 v199, v200, v198
	v_cndmask_b32_e64 v200, v153, v165, s[18:19]
	v_mul_f32_e32 v198, 0x3e000000, v199
	s_waitcnt lgkmcnt(0)
	v_mul_f32_e32 v196, v200, v196
	v_cndmask_b32_e64 v198, v199, v198, s[28:29]
	v_cndmask_b32_e64 v199, v126, v164, s[18:19]
	v_cndmask_b32_e64 v196, v196, -v196, vcc
	v_fmac_f32_e32 v196, v199, v187
	v_mul_f32_e32 v187, 0x3e000000, v196
	v_cndmask_b32_e64 v187, v196, v187, s[28:29]
	v_cvt_pk_bf16_f32 v187, v198, v187
	global_store_dwordx4 v[192:193], v[184:187], off
	s_waitcnt vmcnt(4)
	v_lshlrev_b32_e32 v193, 16, v191
	v_lshlrev_b32_e32 v192, 16, v190
	v_and_b32_e32 v187, 0xffff0000, v189
	v_and_b32_e32 v186, 0xffff0000, v188
	v_lshlrev_b32_e32 v185, 16, v189
	v_lshlrev_b32_e32 v184, 16, v188
	v_pk_mul_f32 v[188:189], v[186:187], v[186:187]
	v_and_b32_e32 v191, 0xffff0000, v191
	v_and_b32_e32 v190, 0xffff0000, v190
	v_pk_fma_f32 v[188:189], v[184:185], v[184:185], v[188:189]
	v_pk_mul_f32 v[194:195], v[190:191], v[190:191]
	v_add_f32_e32 v188, v188, v189
	v_pk_fma_f32 v[194:195], v[192:193], v[192:193], v[194:195]
	s_nop 0
	v_add_f32_e32 v188, v194, v188
	v_add_f32_e32 v188, v195, v188
	ds_bpermute_b32 v189, v98, v188
	v_cndmask_b32_e64 v195, v171, v183, s[20:21]
	v_cndmask_b32_e64 v194, v170, v182, s[20:21]
	s_waitcnt lgkmcnt(0)
	v_add_f32_e32 v188, v188, v189
	ds_bpermute_b32 v189, v99, v188
	s_waitcnt lgkmcnt(0)
	v_add_f32_e32 v188, v188, v189
	ds_bpermute_b32 v189, v100, v188
	s_waitcnt lgkmcnt(0)
	v_add_f32_e32 v188, v188, v189
	v_fmamk_f32 v188, v188, 0x3c800000, v212
	v_cmp_gt_f32_e64 s[42:43], s52, v188
	v_mul_f32_e32 v189, 0x4b800000, v188
	s_nop 0
	v_cndmask_b32_e64 v188, v188, v189, s[42:43]
	v_rsq_f32_e32 v188, v188
	s_nop 0
	v_mul_f32_e32 v189, 0x45800000, v188
	v_cndmask_b32_e64 v188, v188, v189, s[42:43]
	v_mul_f32_e32 v184, v188, v184
	v_mul_f32_e32 v184, v109, v184
	ds_bpermute_b32 v189, v100, v184
	v_mul_f32_e32 v186, v188, v186
	v_mul_f32_e32 v186, v110, v186
	v_mul_f32_e32 v185, v188, v185
	v_mul_f32_e32 v185, v111, v185
	s_waitcnt lgkmcnt(0)
	v_mul_f32_e32 v189, v195, v189
	v_cndmask_b32_e64 v189, v189, -v189, vcc
	v_fmac_f32_e32 v189, v194, v184
	v_mul_f32_e32 v184, 0x3e000000, v189
	v_cndmask_b32_e64 v184, v189, v184, s[30:31]
	ds_bpermute_b32 v189, v100, v186
	v_cndmask_b32_e64 v195, v167, v181, s[20:21]
	v_cndmask_b32_e64 v194, v166, v180, s[20:21]
	v_mul_f32_e32 v187, v188, v187
	v_mul_f32_e32 v187, v112, v187
	s_waitcnt lgkmcnt(0)
	v_mul_f32_e32 v189, v195, v189
	v_cndmask_b32_e64 v189, v189, -v189, vcc
	v_fmac_f32_e32 v189, v194, v186
	v_mul_f32_e32 v186, 0x3e000000, v189
	v_cndmask_b32_e64 v186, v189, v186, s[30:31]
	ds_bpermute_b32 v189, v100, v185
	v_cndmask_b32_e64 v195, v163, v179, s[20:21]
	v_cndmask_b32_e64 v194, v162, v178, s[20:21]
	v_mul_f32_e32 v190, v188, v190
	v_mul_f32_e32 v190, v114, v190
	s_waitcnt lgkmcnt(0)
	v_mul_f32_e32 v189, v195, v189
	v_cndmask_b32_e64 v189, v189, -v189, vcc
	v_fmac_f32_e32 v189, v194, v185
	v_mul_f32_e32 v185, 0x3e000000, v189
	v_cndmask_b32_e64 v185, v189, v185, s[30:31]
	ds_bpermute_b32 v189, v100, v187
	v_cndmask_b32_e64 v195, v161, v177, s[20:21]
	v_cndmask_b32_e64 v194, v160, v176, s[20:21]
	v_cvt_pk_bf16_f32 v184, v184, v186
	s_waitcnt lgkmcnt(0)
	v_mul_f32_e32 v189, v195, v189
	v_cndmask_b32_e64 v189, v189, -v189, vcc
	v_fmac_f32_e32 v189, v194, v187
	v_mul_f32_e32 v187, 0x3e000000, v189
	v_cndmask_b32_e64 v187, v189, v187, s[30:31]
	v_mul_f32_e32 v189, v188, v192
	v_mul_f32_e32 v189, v113, v189
	ds_bpermute_b32 v192, v100, v189
	v_cndmask_b32_e64 v195, v159, v175, s[20:21]
	v_cndmask_b32_e64 v194, v158, v174, s[20:21]
	v_cvt_pk_bf16_f32 v185, v185, v187
	s_waitcnt lgkmcnt(0)
	v_mul_f32_e32 v192, v195, v192
	v_cndmask_b32_e64 v192, v192, -v192, vcc
	v_fmac_f32_e32 v192, v194, v189
	v_mul_f32_e32 v189, 0x3e000000, v192
	v_cndmask_b32_e64 v189, v192, v189, s[30:31]
	ds_bpermute_b32 v192, v100, v190
	v_cndmask_b32_e64 v195, v157, v173, s[20:21]
	v_cndmask_b32_e64 v194, v156, v172, s[20:21]
	s_waitcnt lgkmcnt(0)
	v_mul_f32_e32 v192, v195, v192
	v_cndmask_b32_e64 v192, v192, -v192, vcc
	v_fmac_f32_e32 v192, v194, v190
	v_mul_f32_e32 v190, 0x3e000000, v192
	v_cndmask_b32_e64 v190, v192, v190, s[30:31]
	v_mul_f32_e32 v192, v188, v193
	v_mul_f32_e32 v192, v115, v192
	ds_bpermute_b32 v193, v100, v192
	v_mul_f32_e32 v188, v188, v191
	v_mul_f32_e32 v188, v116, v188
	ds_bpermute_b32 v191, v100, v188
	v_cndmask_b32_e64 v195, v155, v169, s[20:21]
	s_waitcnt lgkmcnt(1)
	v_mul_f32_e32 v193, v195, v193
	v_cndmask_b32_e64 v194, v154, v168, s[20:21]
	v_cndmask_b32_e64 v193, v193, -v193, vcc
	v_fmac_f32_e32 v193, v194, v192
	v_cndmask_b32_e64 v194, v153, v165, s[20:21]
	v_mul_f32_e32 v192, 0x3e000000, v193
	s_waitcnt lgkmcnt(0)
	v_mul_f32_e32 v191, v194, v191
	v_cndmask_b32_e64 v192, v193, v192, s[30:31]
	v_cndmask_b32_e64 v193, v126, v164, s[20:21]
	v_cndmask_b32_e64 v191, v191, -v191, vcc
	v_fmac_f32_e32 v191, v193, v188
	v_mul_f32_e32 v188, 0x3e000000, v191
	v_cndmask_b32_e64 v188, v191, v188, s[30:31]
	v_cvt_pk_bf16_f32 v186, v189, v190
	v_cvt_pk_bf16_f32 v187, v192, v188
	global_store_dwordx4 v[94:95], v[184:187], off
	s_waitcnt vmcnt(4)
	v_lshlrev_b32_e32 v95, 16, v43
	v_lshlrev_b32_e32 v94, 16, v42
	v_and_b32_e32 v43, 0xffff0000, v43
	v_and_b32_e32 v42, 0xffff0000, v42
	v_pk_mul_f32 v[184:185], v[42:43], v[42:43]
	v_lshlrev_b32_e32 v187, 16, v45
	v_lshlrev_b32_e32 v186, 16, v44
	v_and_b32_e32 v45, 0xffff0000, v45
	v_and_b32_e32 v44, 0xffff0000, v44
	v_pk_fma_f32 v[184:185], v[94:95], v[94:95], v[184:185]
	v_pk_mul_f32 v[188:189], v[44:45], v[44:45]
	v_add_f32_e32 v184, v184, v185
	v_pk_fma_f32 v[188:189], v[186:187], v[186:187], v[188:189]
	s_nop 0
	v_add_f32_e32 v184, v188, v184
	v_add_f32_e32 v184, v189, v184
	ds_bpermute_b32 v185, v98, v184
	v_cndmask_b32_e64 v189, v171, v183, s[22:23]
	v_cndmask_b32_e64 v188, v170, v182, s[22:23]
	s_waitcnt lgkmcnt(0)
	v_add_f32_e32 v184, v184, v185
	ds_bpermute_b32 v185, v99, v184
	s_waitcnt lgkmcnt(0)
	v_add_f32_e32 v184, v184, v185
	ds_bpermute_b32 v185, v100, v184
	s_waitcnt lgkmcnt(0)
	v_add_f32_e32 v184, v184, v185
	v_fmamk_f32 v184, v184, 0x3c800000, v212
	v_cmp_gt_f32_e64 s[42:43], s52, v184
	v_mul_f32_e32 v185, 0x4b800000, v184
	s_nop 0
	v_cndmask_b32_e64 v184, v184, v185, s[42:43]
	v_rsq_f32_e32 v184, v184
	s_nop 0
	v_mul_f32_e32 v185, 0x45800000, v184
	v_cndmask_b32_e64 v184, v184, v185, s[42:43]
	v_mul_f32_e32 v94, v184, v94
	v_mul_f32_e32 v94, v117, v94
	ds_bpermute_b32 v185, v100, v94
	v_mul_f32_e32 v42, v184, v42
	v_mul_f32_e32 v42, v118, v42
	v_mul_f32_e32 v95, v184, v95
	v_mul_f32_e32 v95, v119, v95
	s_waitcnt lgkmcnt(0)
	v_mul_f32_e32 v185, v189, v185
	v_cndmask_b32_e64 v185, v185, -v185, vcc
	v_fmac_f32_e32 v185, v188, v94
	v_mul_f32_e32 v94, 0x3e000000, v185
	v_cndmask_b32_e64 v94, v185, v94, s[34:35]
	ds_bpermute_b32 v185, v100, v42
	v_cndmask_b32_e64 v189, v167, v181, s[22:23]
	v_cndmask_b32_e64 v188, v166, v180, s[22:23]
	v_mul_f32_e32 v43, v184, v43
	v_mul_f32_e32 v43, v120, v43
	s_waitcnt lgkmcnt(0)
	v_mul_f32_e32 v185, v189, v185
	v_cndmask_b32_e64 v185, v185, -v185, vcc
	v_fmac_f32_e32 v185, v188, v42
	v_mul_f32_e32 v42, 0x3e000000, v185
	v_cndmask_b32_e64 v42, v185, v42, s[34:35]
	ds_bpermute_b32 v185, v100, v95
	v_cndmask_b32_e64 v189, v163, v179, s[22:23]
	v_cndmask_b32_e64 v188, v162, v178, s[22:23]
	v_mul_f32_e32 v44, v184, v44
	v_mul_f32_e32 v44, v134, v44
	s_waitcnt lgkmcnt(0)
	v_mul_f32_e32 v185, v189, v185
	v_cndmask_b32_e64 v185, v185, -v185, vcc
	v_fmac_f32_e32 v185, v188, v95
	v_mul_f32_e32 v95, 0x3e000000, v185
	v_cndmask_b32_e64 v95, v185, v95, s[34:35]
	ds_bpermute_b32 v185, v100, v43
	v_cndmask_b32_e64 v189, v161, v177, s[22:23]
	v_cndmask_b32_e64 v188, v160, v176, s[22:23]
	v_mul_f32_e32 v45, v184, v45
	v_mul_f32_e32 v45, v136, v45
	s_waitcnt lgkmcnt(0)
	v_mul_f32_e32 v185, v189, v185
	v_cndmask_b32_e64 v185, v185, -v185, vcc
	v_fmac_f32_e32 v185, v188, v43
	v_mul_f32_e32 v43, 0x3e000000, v185
	v_cndmask_b32_e64 v43, v185, v43, s[34:35]
	v_mul_f32_e32 v185, v184, v186
	v_mul_f32_e32 v185, v121, v185
	ds_bpermute_b32 v186, v100, v185
	v_cndmask_b32_e64 v189, v159, v175, s[22:23]
	v_cndmask_b32_e64 v188, v158, v174, s[22:23]
	v_cvt_pk_bf16_f32 v42, v94, v42
	v_cvt_pk_bf16_f32 v43, v95, v43
	s_waitcnt lgkmcnt(0)
	v_mul_f32_e32 v186, v189, v186
	v_cndmask_b32_e64 v186, v186, -v186, vcc
	v_fmac_f32_e32 v186, v188, v185
	v_mul_f32_e32 v185, 0x3e000000, v186
	v_cndmask_b32_e64 v185, v186, v185, s[34:35]
	ds_bpermute_b32 v186, v100, v44
	v_cndmask_b32_e64 v189, v157, v173, s[22:23]
	v_cndmask_b32_e64 v188, v156, v172, s[22:23]
	s_waitcnt lgkmcnt(0)
	v_mul_f32_e32 v186, v189, v186
	v_cndmask_b32_e64 v186, v186, -v186, vcc
	v_fmac_f32_e32 v186, v188, v44
	v_mul_f32_e32 v44, 0x3e000000, v186
	v_cndmask_b32_e64 v44, v186, v44, s[34:35]
	v_mul_f32_e32 v186, v184, v187
	v_mul_f32_e32 v186, v135, v186
	ds_bpermute_b32 v187, v100, v186
	ds_bpermute_b32 v184, v100, v45
	v_cndmask_b32_e64 v189, v155, v169, s[22:23]
	v_cndmask_b32_e64 v188, v154, v168, s[22:23]
	v_cvt_pk_bf16_f32 v44, v185, v44
	s_waitcnt lgkmcnt(1)
	v_mul_f32_e32 v187, v189, v187
	v_cndmask_b32_e64 v187, v187, -v187, vcc
	v_fmac_f32_e32 v187, v188, v186
	v_cndmask_b32_e64 v188, v153, v165, s[22:23]
	v_mul_f32_e32 v186, 0x3e000000, v187
	s_waitcnt lgkmcnt(0)
	v_mul_f32_e32 v184, v188, v184
	v_cndmask_b32_e64 v186, v187, v186, s[34:35]
	v_cndmask_b32_e64 v187, v126, v164, s[22:23]
	v_cndmask_b32_e64 v184, v184, -v184, vcc
	v_fmac_f32_e32 v184, v187, v45
	v_mul_f32_e32 v45, 0x3e000000, v184
	v_cndmask_b32_e64 v45, v184, v45, s[34:35]
	v_cvt_pk_bf16_f32 v45, v186, v45
	global_store_dwordx4 v[92:93], v[42:45], off
	s_waitcnt vmcnt(4)
	v_lshlrev_b32_e32 v93, 16, v41
	v_lshlrev_b32_e32 v92, 16, v40
	v_lshlrev_b32_e32 v43, 16, v39
	v_lshlrev_b32_e32 v42, 16, v38
	v_and_b32_e32 v39, 0xffff0000, v39
	v_and_b32_e32 v38, 0xffff0000, v38
	v_pk_mul_f32 v[44:45], v[38:39], v[38:39]
	v_and_b32_e32 v41, 0xffff0000, v41
	v_and_b32_e32 v40, 0xffff0000, v40
	v_pk_fma_f32 v[44:45], v[42:43], v[42:43], v[44:45]
	v_pk_mul_f32 v[94:95], v[40:41], v[40:41]
	v_add_f32_e32 v44, v44, v45
	v_pk_fma_f32 v[94:95], v[92:93], v[92:93], v[94:95]
	s_nop 0
	v_add_f32_e32 v44, v94, v44
	v_add_f32_e32 v44, v95, v44
	ds_bpermute_b32 v45, v98, v44
	v_cndmask_b32_e64 v95, v171, v183, s[24:25]
	v_cndmask_b32_e64 v94, v170, v182, s[24:25]
	s_waitcnt lgkmcnt(0)
	v_add_f32_e32 v44, v44, v45
	ds_bpermute_b32 v45, v99, v44
	s_waitcnt lgkmcnt(0)
	v_add_f32_e32 v44, v44, v45
	ds_bpermute_b32 v45, v100, v44
	s_waitcnt lgkmcnt(0)
	v_add_f32_e32 v44, v44, v45
	v_fmamk_f32 v44, v44, 0x3c800000, v212
	v_cmp_gt_f32_e64 s[42:43], s52, v44
	v_mul_f32_e32 v45, 0x4b800000, v44
	s_nop 0
	v_cndmask_b32_e64 v44, v44, v45, s[42:43]
	v_rsq_f32_e32 v44, v44
	s_nop 0
	v_mul_f32_e32 v45, 0x45800000, v44
	v_cndmask_b32_e64 v44, v44, v45, s[42:43]
	v_mul_f32_e32 v42, v44, v42
	v_mul_f32_e32 v42, v137, v42
	ds_bpermute_b32 v45, v100, v42
	v_mul_f32_e32 v38, v44, v38
	v_mul_f32_e32 v38, v138, v38
	v_mul_f32_e32 v43, v44, v43
	v_mul_f32_e32 v43, v139, v43
	s_waitcnt lgkmcnt(0)
	v_mul_f32_e32 v45, v95, v45
	v_cndmask_b32_e64 v45, v45, -v45, vcc
	v_fmac_f32_e32 v45, v94, v42
	v_mul_f32_e32 v42, 0x3e000000, v45
	v_cndmask_b32_e64 v42, v45, v42, s[36:37]
	ds_bpermute_b32 v45, v100, v38
	v_cndmask_b32_e64 v95, v167, v181, s[24:25]
	v_cndmask_b32_e64 v94, v166, v180, s[24:25]
	v_mul_f32_e32 v39, v44, v39
	v_mul_f32_e32 v39, v140, v39
	s_waitcnt lgkmcnt(0)
	v_mul_f32_e32 v45, v95, v45
	v_cndmask_b32_e64 v45, v45, -v45, vcc
	v_fmac_f32_e32 v45, v94, v38
	v_mul_f32_e32 v38, 0x3e000000, v45
	v_cndmask_b32_e64 v38, v45, v38, s[36:37]
	ds_bpermute_b32 v45, v100, v43
	v_cndmask_b32_e64 v95, v163, v179, s[24:25]
	v_cndmask_b32_e64 v94, v162, v178, s[24:25]
	v_mul_f32_e32 v40, v44, v40
	v_mul_f32_e32 v40, v142, v40
	s_waitcnt lgkmcnt(0)
	v_mul_f32_e32 v45, v95, v45
	v_cndmask_b32_e64 v45, v45, -v45, vcc
	v_fmac_f32_e32 v45, v94, v43
	v_mul_f32_e32 v43, 0x3e000000, v45
	v_cndmask_b32_e64 v43, v45, v43, s[36:37]
	ds_bpermute_b32 v45, v100, v39
	v_cndmask_b32_e64 v95, v161, v177, s[24:25]
	v_cndmask_b32_e64 v94, v160, v176, s[24:25]
	v_mul_f32_e32 v41, v44, v41
	v_mul_f32_e32 v41, v144, v41
	s_waitcnt lgkmcnt(0)
	v_mul_f32_e32 v45, v95, v45
	v_cndmask_b32_e64 v45, v45, -v45, vcc
	v_fmac_f32_e32 v45, v94, v39
	v_mul_f32_e32 v39, 0x3e000000, v45
	v_cndmask_b32_e64 v39, v45, v39, s[36:37]
	v_mul_f32_e32 v45, v44, v92
	v_mul_f32_e32 v45, v141, v45
	ds_bpermute_b32 v92, v100, v45
	v_cndmask_b32_e64 v95, v159, v175, s[24:25]
	v_cndmask_b32_e64 v94, v158, v174, s[24:25]
	v_cvt_pk_bf16_f32 v38, v42, v38
	v_cvt_pk_bf16_f32 v39, v43, v39
	s_waitcnt lgkmcnt(0)
	v_mul_f32_e32 v92, v95, v92
	v_cndmask_b32_e64 v92, v92, -v92, vcc
	v_fmac_f32_e32 v92, v94, v45
	v_mul_f32_e32 v45, 0x3e000000, v92
	v_cndmask_b32_e64 v45, v92, v45, s[36:37]
	ds_bpermute_b32 v92, v100, v40
	v_cndmask_b32_e64 v95, v157, v173, s[24:25]
	v_cndmask_b32_e64 v94, v156, v172, s[24:25]
	v_lshlrev_b64 v[42:43], v60, v[90:91]
	v_lshl_add_u64 v[42:43], v[62:63], 0, v[42:43]
	s_waitcnt lgkmcnt(0)
	v_mul_f32_e32 v92, v95, v92
	v_cndmask_b32_e64 v92, v92, -v92, vcc
	v_fmac_f32_e32 v92, v94, v40
	v_mul_f32_e32 v40, 0x3e000000, v92
	v_cndmask_b32_e64 v40, v92, v40, s[36:37]
	v_mul_f32_e32 v92, v44, v93
	v_mul_f32_e32 v92, v143, v92
	ds_bpermute_b32 v93, v100, v92
	ds_bpermute_b32 v44, v100, v41
	v_cndmask_b32_e64 v95, v155, v169, s[24:25]
	v_cndmask_b32_e64 v94, v154, v168, s[24:25]
	v_cvt_pk_bf16_f32 v40, v45, v40
	s_waitcnt lgkmcnt(1)
	v_mul_f32_e32 v93, v95, v93
	v_cndmask_b32_e64 v93, v93, -v93, vcc
	v_fmac_f32_e32 v93, v94, v92
	v_cndmask_b32_e64 v94, v153, v165, s[24:25]
	v_mul_f32_e32 v92, 0x3e000000, v93
	s_waitcnt lgkmcnt(0)
	v_mul_f32_e32 v44, v94, v44
	v_cndmask_b32_e64 v92, v93, v92, s[36:37]
	v_cndmask_b32_e64 v93, v126, v164, s[24:25]
	v_cndmask_b32_e64 v44, v44, -v44, vcc
	v_fmac_f32_e32 v44, v93, v41
	v_mul_f32_e32 v41, 0x3e000000, v44
	v_cndmask_b32_e64 v41, v44, v41, s[36:37]
	v_cvt_pk_bf16_f32 v41, v92, v41
	global_store_dwordx4 v[42:43], v[38:41], off
	s_waitcnt vmcnt(4)
	v_lshlrev_b32_e32 v43, 16, v37
	v_lshlrev_b32_e32 v42, 16, v36
	v_lshlrev_b32_e32 v39, 16, v35
	v_lshlrev_b32_e32 v38, 16, v34
	v_and_b32_e32 v35, 0xffff0000, v35
	v_and_b32_e32 v34, 0xffff0000, v34
	v_pk_mul_f32 v[40:41], v[34:35], v[34:35]
	v_and_b32_e32 v37, 0xffff0000, v37
	v_and_b32_e32 v36, 0xffff0000, v36
	v_pk_fma_f32 v[40:41], v[38:39], v[38:39], v[40:41]
	v_pk_mul_f32 v[44:45], v[36:37], v[36:37]
	v_add_f32_e32 v40, v40, v41
	v_pk_fma_f32 v[44:45], v[42:43], v[42:43], v[44:45]
	s_nop 0
	v_add_f32_e32 v40, v44, v40
	v_add_f32_e32 v40, v45, v40
	ds_bpermute_b32 v41, v98, v40
	v_cndmask_b32_e64 v45, v171, v183, s[26:27]
	v_cndmask_b32_e64 v44, v170, v182, s[26:27]
	s_waitcnt lgkmcnt(0)
	v_add_f32_e32 v40, v40, v41
	ds_bpermute_b32 v41, v99, v40
	s_waitcnt lgkmcnt(0)
	v_add_f32_e32 v40, v40, v41
	ds_bpermute_b32 v41, v100, v40
	s_waitcnt lgkmcnt(0)
	v_add_f32_e32 v40, v40, v41
	v_fmamk_f32 v40, v40, 0x3c800000, v212
	v_cmp_gt_f32_e64 s[42:43], s52, v40
	v_mul_f32_e32 v41, 0x4b800000, v40
	s_nop 0
	v_cndmask_b32_e64 v40, v40, v41, s[42:43]
	v_rsq_f32_e32 v40, v40
	s_nop 0
	v_mul_f32_e32 v41, 0x45800000, v40
	v_cndmask_b32_e64 v40, v40, v41, s[42:43]
	v_mul_f32_e32 v38, v40, v38
	v_mul_f32_e32 v38, v145, v38
	ds_bpermute_b32 v41, v100, v38
	v_mul_f32_e32 v34, v40, v34
	v_mul_f32_e32 v34, v146, v34
	v_mul_f32_e32 v39, v40, v39
	v_mul_f32_e32 v39, v147, v39
	s_waitcnt lgkmcnt(0)
	v_mul_f32_e32 v41, v45, v41
	v_cndmask_b32_e64 v41, v41, -v41, vcc
	v_fmac_f32_e32 v41, v44, v38
	v_mul_f32_e32 v38, 0x3e000000, v41
	v_cndmask_b32_e64 v38, v41, v38, s[38:39]
	ds_bpermute_b32 v41, v100, v34
	v_cndmask_b32_e64 v45, v167, v181, s[26:27]
	v_cndmask_b32_e64 v44, v166, v180, s[26:27]
	v_mul_f32_e32 v35, v40, v35
	v_mul_f32_e32 v35, v148, v35
	s_waitcnt lgkmcnt(0)
	v_mul_f32_e32 v41, v45, v41
	v_cndmask_b32_e64 v41, v41, -v41, vcc
	v_fmac_f32_e32 v41, v44, v34
	v_mul_f32_e32 v34, 0x3e000000, v41
	v_cndmask_b32_e64 v34, v41, v34, s[38:39]
	ds_bpermute_b32 v41, v100, v39
	v_cndmask_b32_e64 v45, v163, v179, s[26:27]
	v_cndmask_b32_e64 v44, v162, v178, s[26:27]
	v_mul_f32_e32 v36, v40, v36
	v_mul_f32_e32 v36, v150, v36
	s_waitcnt lgkmcnt(0)
	v_mul_f32_e32 v41, v45, v41
	v_cndmask_b32_e64 v41, v41, -v41, vcc
	v_fmac_f32_e32 v41, v44, v39
	v_mul_f32_e32 v39, 0x3e000000, v41
	v_cndmask_b32_e64 v39, v41, v39, s[38:39]
	ds_bpermute_b32 v41, v100, v35
	v_cndmask_b32_e64 v45, v161, v177, s[26:27]
	v_cndmask_b32_e64 v44, v160, v176, s[26:27]
	v_mul_f32_e32 v37, v40, v37
	v_mul_f32_e32 v37, v152, v37
	s_waitcnt lgkmcnt(0)
	v_mul_f32_e32 v41, v45, v41
	v_cndmask_b32_e64 v41, v41, -v41, vcc
	v_fmac_f32_e32 v41, v44, v35
	v_mul_f32_e32 v35, 0x3e000000, v41
	v_cndmask_b32_e64 v35, v41, v35, s[38:39]
	v_mul_f32_e32 v41, v40, v42
	v_mul_f32_e32 v41, v149, v41
	ds_bpermute_b32 v42, v100, v41
	v_cndmask_b32_e64 v45, v159, v175, s[26:27]
	v_cndmask_b32_e64 v44, v158, v174, s[26:27]
	v_cvt_pk_bf16_f32 v34, v38, v34
	v_cvt_pk_bf16_f32 v35, v39, v35
	s_waitcnt lgkmcnt(0)
	v_mul_f32_e32 v42, v45, v42
	v_cndmask_b32_e64 v42, v42, -v42, vcc
	v_fmac_f32_e32 v42, v44, v41
	v_mul_f32_e32 v41, 0x3e000000, v42
	v_cndmask_b32_e64 v41, v42, v41, s[38:39]
	ds_bpermute_b32 v42, v100, v36
	v_cndmask_b32_e64 v45, v157, v173, s[26:27]
	v_cndmask_b32_e64 v44, v156, v172, s[26:27]
	v_lshlrev_b64 v[38:39], v64, v[88:89]
	v_lshl_add_u64 v[38:39], v[66:67], 0, v[38:39]
	s_waitcnt lgkmcnt(0)
	v_mul_f32_e32 v42, v45, v42
	v_cndmask_b32_e64 v42, v42, -v42, vcc
	v_fmac_f32_e32 v42, v44, v36
	v_mul_f32_e32 v36, 0x3e000000, v42
	v_cndmask_b32_e64 v36, v42, v36, s[38:39]
	v_mul_f32_e32 v42, v40, v43
	v_mul_f32_e32 v42, v151, v42
	ds_bpermute_b32 v43, v100, v42
	ds_bpermute_b32 v40, v100, v37
	v_cndmask_b32_e64 v45, v155, v169, s[26:27]
	v_cndmask_b32_e64 v44, v154, v168, s[26:27]
	v_cvt_pk_bf16_f32 v36, v41, v36
	s_waitcnt lgkmcnt(1)
	v_mul_f32_e32 v43, v45, v43
	v_cndmask_b32_e64 v43, v43, -v43, vcc
	v_fmac_f32_e32 v43, v44, v42
	v_cndmask_b32_e64 v44, v153, v165, s[26:27]
	v_mul_f32_e32 v42, 0x3e000000, v43
	s_waitcnt lgkmcnt(0)
	v_mul_f32_e32 v40, v44, v40
	v_cndmask_b32_e64 v42, v43, v42, s[38:39]
	v_cndmask_b32_e64 v43, v126, v164, s[26:27]
	v_cndmask_b32_e64 v40, v40, -v40, vcc
	v_fmac_f32_e32 v40, v43, v37
	v_mul_f32_e32 v37, 0x3e000000, v40
	v_cndmask_b32_e64 v37, v40, v37, s[38:39]
	v_cvt_pk_bf16_f32 v37, v42, v37
	global_store_dwordx4 v[38:39], v[34:37], off
	s_cbranch_scc0 .LBB0_449
	s_and_saveexec_b64 s[18:19], s[4:5]
	s_cbranch_execz .LBB0_435
	v_mov_b32_e32 v36, v0
	s_lshl_b32 s70, s70, 1
	v_lshrrev_b32_e32 v34, 6, v36
	v_and_or_b32 v34, v34, 3, s89
	v_ashrrev_i32_e32 v35, 31, v34
	v_lshlrev_b64 v[34:35], 18, v[34:35]
	v_lshlrev_b32_e32 v37, 12, v36
	v_lshl_add_u64 v[34:35], s[68:69], 0, v[34:35]
	v_and_b32_e32 v126, 0x38000, v37
	v_and_b32_e32 v36, 7, v36
	v_lshl_add_u64 v[34:35], v[34:35], 0, v[126:127]
	v_lshlrev_b32_e32 v36, 3, v36
	v_lshl_add_u64 v[34:35], v[34:35], 0, s[70:71]
	v_ashrrev_i32_e32 v37, 31, v36
	v_lshl_add_u64 v[38:39], v[36:37], 1, v[34:35]
	v_lshlrev_b32_e32 v34, 16, v6
	v_and_b32_e32 v35, 0xffff, v10
	v_and_b32_e32 v36, 0xffff, v18
	v_and_b32_e32 v37, 0xffff, v26
	v_and_or_b32 v34, v2, s94, v34
	v_lshl_or_b32 v35, v14, 16, v35
	v_lshl_or_b32 v36, v22, 16, v36
	v_lshl_or_b32 v37, v30, 16, v37
	global_store_dwordx4 v[38:39], v[34:37], off
	v_add_co_u32_e32 v40, vcc, s96, v38
	s_nop 0
	v_lshrrev_b32_e32 v34, 16, v2
	v_lshrrev_b32_e32 v35, 16, v10
	v_lshrrev_b32_e32 v36, 16, v18
	v_lshrrev_b32_e32 v37, 16, v26
	v_and_or_b32 v34, v6, s95, v34
	v_and_or_b32 v35, v14, s95, v35
	v_and_or_b32 v36, v22, s95, v36
	v_and_or_b32 v37, v30, s95, v37
	v_addc_co_u32_e32 v41, vcc, 0, v39, vcc
	global_store_dwordx4 v[40:41], v[34:37], off offset:-4096
	s_nop 1
	v_lshlrev_b32_e32 v34, 16, v7
	v_and_b32_e32 v35, 0xffff, v11
	v_and_b32_e32 v36, 0xffff, v19
	v_and_b32_e32 v37, 0xffff, v27
	v_and_or_b32 v34, v3, s94, v34
	v_lshl_or_b32 v35, v15, 16, v35
	v_lshl_or_b32 v36, v23, 16, v36
	v_lshl_or_b32 v37, v31, 16, v37
	global_store_dwordx4 v[40:41], v[34:37], off
	v_add_co_u32_e32 v40, vcc, s97, v38
	s_nop 0
	v_lshrrev_b32_e32 v34, 16, v3
	v_lshrrev_b32_e32 v35, 16, v11
	v_lshrrev_b32_e32 v36, 16, v19
	v_lshrrev_b32_e32 v37, 16, v27
	v_and_or_b32 v34, v7, s95, v34
	v_and_or_b32 v35, v15, s95, v35
	v_and_or_b32 v36, v23, s95, v36
	v_and_or_b32 v37, v31, s95, v37
	v_addc_co_u32_e32 v41, vcc, 0, v39, vcc
	global_store_dwordx4 v[40:41], v[34:37], off offset:-4096
	s_nop 1
	v_lshlrev_b32_e32 v34, 16, v8
	v_and_b32_e32 v35, 0xffff, v12
	v_and_b32_e32 v36, 0xffff, v20
	v_and_b32_e32 v37, 0xffff, v28
	v_and_or_b32 v34, v4, s94, v34
	v_lshl_or_b32 v35, v16, 16, v35
	v_lshl_or_b32 v36, v24, 16, v36
	v_lshl_or_b32 v37, v32, 16, v37
	global_store_dwordx4 v[40:41], v[34:37], off
	v_add_co_u32_e32 v40, vcc, s54, v38
	s_nop 0
	v_lshrrev_b32_e32 v34, 16, v4
	v_lshrrev_b32_e32 v35, 16, v12
	v_lshrrev_b32_e32 v36, 16, v20
	v_lshrrev_b32_e32 v37, 16, v28
	v_and_or_b32 v34, v8, s95, v34
	v_and_or_b32 v35, v16, s95, v35
	v_and_or_b32 v36, v24, s95, v36
	v_and_or_b32 v37, v32, s95, v37
	v_addc_co_u32_e32 v41, vcc, 0, v39, vcc
	global_store_dwordx4 v[40:41], v[34:37], off offset:-4096
	v_add_co_u32_e32 v38, vcc, 0x7000, v38
	s_nop 0
	v_lshlrev_b32_e32 v34, 16, v9
	v_and_b32_e32 v35, 0xffff, v13
	v_and_b32_e32 v36, 0xffff, v21
	v_and_b32_e32 v37, 0xffff, v29
	v_and_or_b32 v34, v5, s94, v34
	v_lshl_or_b32 v35, v17, 16, v35
	v_lshl_or_b32 v36, v25, 16, v36
	v_lshl_or_b32 v37, v33, 16, v37
	global_store_dwordx4 v[40:41], v[34:37], off
	v_addc_co_u32_e32 v39, vcc, 0, v39, vcc
	s_nop 0
	v_lshrrev_b32_e32 v34, 16, v5
	v_lshrrev_b32_e32 v35, 16, v13
	v_lshrrev_b32_e32 v36, 16, v21
	v_lshrrev_b32_e32 v37, 16, v29
	v_and_or_b32 v34, v9, s95, v34
	v_and_or_b32 v35, v17, s95, v35
	v_and_or_b32 v36, v25, s95, v36
	v_and_or_b32 v37, v33, s95, v37
	global_store_dwordx4 v[38:39], v[34:37], off
	s_branch .LBB0_435
